# conv+SiLU phase: row items walked from last to first (most recently written rows first)
# speedup vs baseline: 1.0057x; 1.0057x over previous
; __device__ __forceinline__ unsigned pk2(float lo, float hi) { return f2bf(lo) | (f2bf(hi) << 16); }
; __device__ __forceinline__ float bflo(unsigned w) { return __uint_as_float(w << 16); }
; __device__ __forceinline__ float bfhi(unsigned w) { return __uint_as_float(w & 0xffff0000u); }
; __device__ __forceinline__ float sigmoidf_(float x) { return frcp_(1.0f + fexp_(-x)); }
; __device__ __forceinline__ void p3_conv(const Args& a, const Frame& F) {
;     ...
;     const int cg = F.tid & 127, sub = F.tid >> 7, c0 = cg * 8;
;     float w0[8], w1[8], w2[8], bb[8];
; #pragma unroll
;     for (int j = 0; j < 8; ++j) { w0[j] = cw[c0 + j]; w1[j] = cw[1024 + c0 + j]; w2[j] = cw[2048 + c0 + j]; bb[j] = cb[c0 + j]; }
;     const float scl = c0 < 512 ? 0.08838834764831845f : 1.0f;
;     const u32x4 z = (u32x4){0u, 0u, 0u, 0u};
;     for (int item = F.bid * 4 + sub; item < TA / 16; item += F.G * 4) {
;         const int r0 = item * 16;
;         const int len = (r0 < T) ? SEQ : CTXL, pos0 = (r0 < T) ? (r0 & (SEQ - 1)) : ((r0 - T) & (CTXL - 1));
;         u32x4 rw[18];
; #pragma unroll
;         for (int i = 0; i < 18; ++i) { const int pos = pos0 + i - 1; rw[i] = (pos >= 0 && pos < len) ? *(const u32x4*)(PQK + (size_t)(r0 + i - 1) * 1024 + c0) : z; }
; #pragma unroll
;         for (int i = 0; i < 16; ++i) {
;             const unsigned wm[4] = {rw[i].x, rw[i].y, rw[i].z, rw[i].w}, wc_[4] = {rw[i + 1].x, rw[i + 1].y, rw[i + 1].z, rw[i + 1].w}, wp[4] = {rw[i + 2].x, rw[i + 2].y, rw[i + 2].z, rw[i + 2].w};
;             float o[8];
; #pragma unroll
;             for (int j = 0; j < 4; ++j) {
;                 const float a0 = bb[2 * j] + bflo(wm[j]) * w0[2 * j] + bflo(wc_[j]) * w1[2 * j] + bflo(wp[j]) * w2[2 * j];
;                 const float a1 = bb[2 * j + 1] + bfhi(wm[j]) * w0[2 * j + 1] + bfhi(wc_[j]) * w1[2 * j + 1] + bfhi(wp[j]) * w2[2 * j + 1];
;                 o[2 * j] = a0 * sigmoidf_(a0) * scl; o[2 * j + 1] = a1 * sigmoidf_(a1) * scl; }
;             u32x4 w; w.x = pk2(o[0], o[1]); w.y = pk2(o[2], o[3]); w.z = pk2(o[4], o[5]); w.w = pk2(o[6], o[7]);
;             *(u32x4*)(QKC + (size_t)(r0 + i) * 1024 + c0) = w;
.LBB0_340:
	s_cmp_lt_i32 s74, 4
	s_cselect_b64 s[4:5], -1, 0
	s_and_b64 s[0:1], s[4:5], s[0:1]
	s_andn2_b64 vcc, exec, s[0:1]
	v_lshrrev_b32_e32 v208, 7, v0
	s_cbranch_vccnz .LBB0_381
	v_lshrrev_b32_e32 v34, 7, v0
	v_lshl_or_b32 v1, s2, 2, v34
	s_movk_i32 s4, 0x1080
	v_cmp_gt_i32_e32 vcc, s4, v1
	s_and_saveexec_b64 s[4:5], vcc
	s_cbranch_execz .LBB0_380
	v_lshlrev_b32_e32 v2, 3, v0
	v_and_b32_e32 v35, 0x3f8, v2
	v_lshlrev_b32_e32 v36, 2, v35
	v_mov_b32_e32 v37, 0
	v_lshl_add_u64 v[30:31], s[54:55], 0, v[36:37]
	s_movk_i32 s10, 0x1000
	v_add_co_u32_e32 v22, vcc, s10, v30
	s_movk_i32 s8, 0x2000
	s_nop 0
	v_addc_co_u32_e32 v23, vcc, 0, v31, vcc
	global_load_dwordx4 v[2:5], v36, s[56:57] offset:16
	global_load_dwordx4 v[6:9], v36, s[56:57]
	s_mov_b64 s[6:7], 0x2000
	global_load_dwordx4 v[10:13], v36, s[54:55]
	global_load_dwordx4 v[14:17], v36, s[54:55] offset:16
	global_load_dwordx4 v[18:21], v[22:23], off nt
	v_add_co_u32_e32 v22, vcc, s8, v30
	s_mov_b64 s[8:9], 0x1000
	s_nop 0
	v_addc_co_u32_e32 v23, vcc, 0, v31, vcc
	v_lshl_add_u64 v[26:27], v[30:31], 0, s[8:9]
	v_lshl_add_u64 v[30:31], v[30:31], 0, s[6:7]
	global_load_dwordx4 v[22:25], v[22:23], off nt
	s_movk_i32 s20, 0x200
	global_load_dwordx4 v[26:29], v[26:27], off offset:16 nt
	v_mov_b32_e32 v36, 0x3db504f3
	global_load_dwordx4 v[30:33], v[30:31], off offset:16 nt
	v_lshlrev_b32_e32 v34, 4, v34
	v_cmp_gt_u32_e32 vcc, s20, v35
	v_lshl_or_b32 v34, s2, 6, v34
	s_mov_b64 s[8:9], 0xac00000
	v_cndmask_b32_e32 v104, 1.0, v36, vcc
	v_lshlrev_b32_e32 v36, 1, v35
	s_mov_b64 s[16:17], 0x2800000
	v_add_u32_e32 v106, -1, v34
	v_cmp_gt_u32_e32 vcc, 0x80, v1
	v_mov_b32_e32 v106, 0xc00
	v_mov_b32_e32 v107, 0x1000
	v_cndmask_b32_e32 v106, v106, v107, vcc
	v_add_u32_e32 v1, v1, v106
	v_lshlrev_b32_e32 v106, 4, v1
	v_add_u32_e32 v106, -1, v106
	v_lshl_add_u64 v[34:35], s[72:73], 0, v[36:37]
	s_lshl_b32 s11, s3, 2
	s_lshl_b32 s12, s3, 6
	s_sub_i32 s11, 0, s11
	s_sub_i32 s12, 0, s12
	s_mov_b64 s[6:7], 0
	s_mov_b32 s13, 0xffff0000
	s_movk_i32 s14, 0x7fff
	s_movk_i32 s15, 0x107f
	v_mov_b32_e32 v146, 0x100
	v_mov_b32_e32 v147, 0x2000
	v_mov_b32_e32 v148, 0xf0
	v_mov_b32_e32 v105, v104
	v_lshl_add_u64 v[108:109], v[34:35], 0, s[8:9]
	v_lshl_add_u64 v[110:111], v[34:35], 0, s[16:17]
	v_mov_b32_e32 v149, 0x1ff0
	s_waitcnt vmcnt(0)
	v_mov_b32_e32 v112, v7
	v_mov_b32_e32 v113, v9
	v_mov_b32_e32 v114, v11
	v_mov_b32_e32 v115, v13
	v_mov_b32_e32 v7, v8
	v_mov_b32_e32 v11, v12
	v_mov_b32_e32 v8, v3
	v_mov_b32_e32 v9, v5
	v_mov_b32_e32 v12, v15
	v_mov_b32_e32 v13, v17
	v_mov_b32_e32 v3, v4
	v_mov_b32_e32 v15, v16
	v_mov_b32_e32 v4, v19
	v_mov_b32_e32 v5, v21
	v_mov_b32_e32 v16, v23
	v_mov_b32_e32 v17, v25
	v_mov_b32_e32 v19, v20
	v_mov_b32_e32 v23, v24
	v_mov_b32_e32 v20, v27
	v_mov_b32_e32 v21, v29
	v_mov_b32_e32 v24, v31
	v_mov_b32_e32 v25, v33
	v_mov_b32_e32 v27, v28
	v_mov_b32_e32 v31, v32
	s_branch .LBB0_344
.LBB0_343:
	s_or_b64 exec, exec, s[8:9]
	s_waitcnt vmcnt(0)
	v_lshlrev_b32_e32 v153, 16, v97
	v_lshlrev_b32_e32 v152, 16, v96
	v_and_b32_e32 v97, 0xffff0000, v97
	v_and_b32_e32 v96, 0xffff0000, v96
	v_lshlrev_b32_e32 v150, 16, v100
	v_and_b32_e32 v100, 0xffff0000, v100
	v_lshlrev_b32_e32 v151, 16, v101
	v_and_b32_e32 v101, 0xffff0000, v101
	v_pk_fma_f32 v[96:97], v[114:115], v[96:97], v[112:113]
	v_pk_fma_f32 v[152:153], v[10:11], v[152:153], v[6:7]
	v_pk_fma_f32 v[96:97], v[4:5], v[100:101], v[96:97]
	v_and_b32_e32 v161, 0xffff0000, v93
	v_and_b32_e32 v160, 0xffff0000, v92
	v_pk_fma_f32 v[152:153], v[18:19], v[150:151], v[152:153]
	v_lshlrev_b32_e32 v159, 16, v93
	v_lshlrev_b32_e32 v158, 16, v92
	v_pk_fma_f32 v[92:93], v[16:17], v[160:161], v[96:97]
	v_pk_fma_f32 v[152:153], v[22:23], v[158:159], v[152:153]
	v_mul_f32_e32 v96, 0xbfb8aa3b, v92
	v_mul_f32_e32 v107, 0xbfb8aa3b, v152
	v_exp_f32_e32 v97, v96
	v_mul_f32_e32 v96, 0xbfb8aa3b, v153
	v_exp_f32_e32 v107, v107
	v_exp_f32_e32 v162, v96
	v_lshlrev_b32_e32 v157, 16, v99
	v_lshlrev_b32_e32 v156, 16, v98
	v_add_f32_e32 v96, 1.0, v107
	v_add_f32_e32 v107, 1.0, v97
	v_add_f32_e32 v97, 1.0, v162
	v_rcp_f32_e32 v96, v96
	v_rcp_f32_e32 v97, v97
	v_mul_f32_e32 v162, 0xbfb8aa3b, v93
	v_exp_f32_e32 v163, v162
	v_lshlrev_b32_e32 v154, 16, v102
	v_lshlrev_b32_e32 v155, 16, v103
	v_pk_mul_f32 v[96:97], v[152:153], v[96:97]
	v_pk_fma_f32 v[152:153], v[14:15], v[156:157], v[2:3]
	v_lshlrev_b32_e32 v157, 16, v95
	v_pk_fma_f32 v[152:153], v[26:27], v[154:155], v[152:153]
	v_lshlrev_b32_e32 v156, 16, v94
	v_rcp_f32_e32 v162, v107
	v_add_f32_e32 v107, 1.0, v163
	v_pk_fma_f32 v[152:153], v[30:31], v[156:157], v[152:153]
	v_and_b32_e32 v99, 0xffff0000, v99
	v_and_b32_e32 v98, 0xffff0000, v98
	v_rcp_f32_e32 v163, v107
	v_mul_f32_e32 v107, 0xbfb8aa3b, v152
	v_and_b32_e32 v102, 0xffff0000, v102
	v_and_b32_e32 v103, 0xffff0000, v103
	v_exp_f32_e32 v107, v107
	v_pk_fma_f32 v[98:99], v[12:13], v[98:99], v[8:9]
	v_and_b32_e32 v165, 0xffff0000, v95
	v_pk_fma_f32 v[98:99], v[20:21], v[102:103], v[98:99]
	v_and_b32_e32 v164, 0xffff0000, v94
	v_pk_fma_f32 v[94:95], v[24:25], v[164:165], v[98:99]
	v_pk_mul_f32 v[92:93], v[92:93], v[162:163]
	v_mul_f32_e32 v98, 0xbfb8aa3b, v94
	v_exp_f32_e32 v99, v98
	v_add_f32_e32 v98, 1.0, v107
	v_mul_f32_e32 v107, 0xbfb8aa3b, v153
	v_mul_f32_e32 v162, 0xbfb8aa3b, v95
	v_exp_f32_e32 v107, v107
	v_exp_f32_e32 v163, v162
	v_add_f32_e32 v99, 1.0, v99
	v_rcp_f32_e32 v162, v99
	v_add_f32_e32 v99, 1.0, v107
	v_add_f32_e32 v107, 1.0, v163
	v_rcp_f32_e32 v163, v107
	v_rcp_f32_e32 v98, v98
	v_rcp_f32_e32 v99, v99
	v_pk_mul_f32 v[96:97], v[104:105], v[96:97]
	v_pk_mul_f32 v[94:95], v[94:95], v[162:163]
	v_pk_mul_f32 v[92:93], v[104:105], v[92:93]
; __device__ __forceinline__ unsigned pk2(float lo, float hi) { return f2bf(lo) | (f2bf(hi) << 16); }
; __device__ __forceinline__ float bflo(unsigned w) { return __uint_as_float(w << 16); }
; __device__ __forceinline__ float bfhi(unsigned w) { return __uint_as_float(w & 0xffff0000u); }
; __device__ __forceinline__ float sigmoidf_(float x) { return frcp_(1.0f + fexp_(-x)); }
; __device__ __forceinline__ void p3_conv(const Args& a, const Frame& F) {
;     ...
;         for (int i = 0; i < 16; ++i) {
;             const unsigned wm[4] = {rw[i].x, rw[i].y, rw[i].z, rw[i].w}, wc_[4] = {rw[i + 1].x, rw[i + 1].y, rw[i + 1].z, rw[i + 1].w}, wp[4] = {rw[i + 2].x, rw[i + 2].y, rw[i + 2].z, rw[i + 2].w};
;             float o[8];
; #pragma unroll
;             for (int j = 0; j < 4; ++j) {
;                 const float a0 = bb[2 * j] + bflo(wm[j]) * w0[2 * j] + bflo(wc_[j]) * w1[2 * j] + bflo(wp[j]) * w2[2 * j];
;                 const float a1 = bb[2 * j + 1] + bfhi(wm[j]) * w0[2 * j + 1] + bfhi(wc_[j]) * w1[2 * j + 1] + bfhi(wp[j]) * w2[2 * j + 1];
;                 o[2 * j] = a0 * sigmoidf_(a0) * scl; o[2 * j + 1] = a1 * sigmoidf_(a1) * scl; }
;             u32x4 w; w.x = pk2(o[0], o[1]); w.y = pk2(o[2], o[3]); w.z = pk2(o[4], o[5]); w.w = pk2(o[6], o[7]);
;             *(u32x4*)(QKC + (size_t)(r0 + i) * 1024 + c0) = w;
	v_pk_mul_f32 v[94:95], v[104:105], v[94:95]
	v_pk_mul_f32 v[98:99], v[152:153], v[98:99]
	v_bfe_u32 v107, v95, 16, 1
	v_bfe_u32 v152, v94, 16, 1
	v_pk_mul_f32 v[98:99], v[104:105], v[98:99]
	v_bfe_u32 v153, v93, 16, 1
	v_bfe_u32 v162, v92, 16, 1
	v_add3_u32 v94, v94, v152, s14
	v_add3_u32 v95, v95, v107, s14
	v_bfe_u32 v107, v96, 16, 1
	v_bfe_u32 v152, v97, 16, 1
	v_add3_u32 v92, v92, v162, s14
	v_add3_u32 v93, v93, v153, s14
	v_bfe_u32 v153, v98, 16, 1
	v_bfe_u32 v162, v99, 16, 1
	v_add3_u32 v97, v97, v152, s14
	v_add3_u32 v96, v96, v107, s14
	v_add3_u32 v99, v99, v162, s14
	v_add3_u32 v98, v98, v153, s14
	v_lshrrev_b32_e32 v96, 16, v96
	v_lshrrev_b32_e32 v97, 16, v97
	v_lshrrev_b32_e32 v98, 16, v98
	v_lshrrev_b32_e32 v99, 16, v99
	v_and_or_b32 v93, v93, s13, v97
	v_and_or_b32 v92, v92, s13, v96
	v_lshlrev_b64 v[96:97], 11, v[144:145]
	v_and_or_b32 v95, v95, s13, v99
	v_and_or_b32 v94, v94, s13, v98
	v_lshl_add_u64 v[96:97], v[110:111], 0, v[96:97]
	global_store_dwordx4 v[96:97], v[92:95], off
	v_and_b32_e32 v99, 0xffff0000, v89
	v_and_b32_e32 v98, 0xffff0000, v88
	v_pk_fma_f32 v[92:93], v[10:11], v[150:151], v[6:7]
	v_lshlrev_b32_e32 v95, 16, v89
	v_pk_fma_f32 v[92:93], v[18:19], v[158:159], v[92:93]
	v_lshlrev_b32_e32 v94, 16, v88
	v_pk_fma_f32 v[92:93], v[22:23], v[94:95], v[92:93]
	v_pk_fma_f32 v[102:103], v[12:13], v[102:103], v[8:9]
	v_mul_f32_e32 v96, 0xbfb8aa3b, v92
	v_exp_f32_e32 v107, v96
	v_pk_fma_f32 v[96:97], v[114:115], v[100:101], v[112:113]
	v_pk_fma_f32 v[102:103], v[20:21], v[164:165], v[102:103]
	v_pk_fma_f32 v[96:97], v[4:5], v[160:161], v[96:97]
	v_and_b32_e32 v151, 0xffff0000, v91
	v_pk_fma_f32 v[88:89], v[16:17], v[98:99], v[96:97]
	v_and_b32_e32 v150, 0xffff0000, v90
	v_mul_f32_e32 v96, 0xbfb8aa3b, v88
	v_exp_f32_e32 v97, v96
	v_mul_f32_e32 v96, 0xbfb8aa3b, v93
	v_exp_f32_e32 v100, v96
	v_add_f32_e32 v96, 1.0, v107
	v_add_f32_e32 v101, 1.0, v97
	v_rcp_f32_e32 v96, v96
	v_add_f32_e32 v97, 1.0, v100
	v_mul_f32_e32 v100, 0xbfb8aa3b, v89
	v_rcp_f32_e32 v97, v97
	v_exp_f32_e32 v107, v100
	v_rcp_f32_e32 v100, v101
	v_lshlrev_b32_e32 v145, 16, v91
	v_pk_mul_f32 v[92:93], v[92:93], v[96:97]
	v_add_f32_e32 v96, 1.0, v107
	v_rcp_f32_e32 v101, v96
	v_pk_fma_f32 v[96:97], v[14:15], v[154:155], v[2:3]
	v_lshlrev_b32_e32 v144, 16, v90
	v_pk_fma_f32 v[90:91], v[24:25], v[150:151], v[102:103]
	v_pk_fma_f32 v[96:97], v[26:27], v[156:157], v[96:97]
	v_mul_f32_e32 v102, 0xbfb8aa3b, v90
	v_pk_fma_f32 v[96:97], v[30:31], v[144:145], v[96:97]
	v_exp_f32_e32 v102, v102
	v_mul_f32_e32 v107, 0xbfb8aa3b, v96
	v_exp_f32_e32 v107, v107
	v_pk_mul_f32 v[88:89], v[88:89], v[100:101]
	v_add_f32_e32 v101, 1.0, v102
	v_mul_f32_e32 v102, 0xbfb8aa3b, v97
	v_exp_f32_e32 v103, v102
	v_mul_f32_e32 v102, 0xbfb8aa3b, v91
	v_add_f32_e32 v100, 1.0, v107
	v_exp_f32_e32 v107, v102
	v_rcp_f32_e32 v102, v101
	v_add_f32_e32 v101, 1.0, v103
	v_rcp_f32_e32 v100, v100
	v_add_f32_e32 v103, 1.0, v107
	v_rcp_f32_e32 v103, v103
	v_rcp_f32_e32 v101, v101
	v_pk_mul_f32 v[92:93], v[104:105], v[92:93]
	v_pk_mul_f32 v[88:89], v[104:105], v[88:89]
	v_pk_mul_f32 v[90:91], v[90:91], v[102:103]
	v_pk_mul_f32 v[96:97], v[96:97], v[100:101]
	v_pk_mul_f32 v[90:91], v[104:105], v[90:91]
	v_pk_mul_f32 v[96:97], v[104:105], v[96:97]
	v_bfe_u32 v100, v91, 16, 1
	v_bfe_u32 v101, v90, 16, 1
	v_bfe_u32 v102, v89, 16, 1
	v_bfe_u32 v103, v88, 16, 1
	v_add3_u32 v90, v90, v101, s14
	v_add3_u32 v91, v91, v100, s14
	v_bfe_u32 v100, v92, 16, 1
	v_bfe_u32 v101, v93, 16, 1
	v_add3_u32 v88, v88, v103, s14
	v_add3_u32 v89, v89, v102, s14
	v_bfe_u32 v102, v96, 16, 1
	v_bfe_u32 v103, v97, 16, 1
	v_add3_u32 v93, v93, v101, s14
	v_add3_u32 v92, v92, v100, s14
	v_add3_u32 v97, v97, v103, s14
	v_add3_u32 v96, v96, v102, s14
	v_lshrrev_b32_e32 v92, 16, v92
	v_lshrrev_b32_e32 v93, 16, v93
	v_lshrrev_b32_e32 v96, 16, v96
	v_lshrrev_b32_e32 v97, 16, v97
	v_and_or_b32 v89, v89, s13, v93
	v_and_or_b32 v88, v88, s13, v92
	v_lshlrev_b64 v[92:93], 11, v[142:143]
	v_and_or_b32 v91, v91, s13, v97
	v_and_or_b32 v90, v90, s13, v96
	v_lshl_add_u64 v[92:93], v[110:111], 0, v[92:93]
	global_store_dwordx4 v[92:93], v[88:91], off
	v_and_b32_e32 v97, 0xffff0000, v85
	v_and_b32_e32 v96, 0xffff0000, v84
	v_pk_fma_f32 v[88:89], v[10:11], v[158:159], v[6:7]
	v_lshlrev_b32_e32 v91, 16, v85
	v_pk_fma_f32 v[88:89], v[18:19], v[94:95], v[88:89]
	v_lshlrev_b32_e32 v90, 16, v84
	v_pk_fma_f32 v[88:89], v[22:23], v[90:91], v[88:89]
	v_pk_fma_f32 v[142:143], v[12:13], v[164:165], v[8:9]
	v_mul_f32_e32 v92, 0xbfb8aa3b, v88
	v_exp_f32_e32 v100, v92
	v_pk_fma_f32 v[92:93], v[114:115], v[160:161], v[112:113]
	v_lshlrev_b32_e32 v103, 16, v87
	v_pk_fma_f32 v[92:93], v[4:5], v[98:99], v[92:93]
	v_lshlrev_b32_e32 v102, 16, v86
	v_pk_fma_f32 v[84:85], v[16:17], v[96:97], v[92:93]
	v_pk_fma_f32 v[142:143], v[20:21], v[150:151], v[142:143]
	v_mul_f32_e32 v92, 0xbfb8aa3b, v84
	v_exp_f32_e32 v93, v92
	v_mul_f32_e32 v92, 0xbfb8aa3b, v89
	v_exp_f32_e32 v101, v92
	v_add_f32_e32 v92, 1.0, v100
	v_add_f32_e32 v100, 1.0, v93
	v_rcp_f32_e32 v92, v92
	v_add_f32_e32 v93, 1.0, v101
	v_mul_f32_e32 v101, 0xbfb8aa3b, v85
	v_rcp_f32_e32 v93, v93
	v_exp_f32_e32 v101, v101
	v_and_b32_e32 v153, 0xffff0000, v87
	v_and_b32_e32 v152, 0xffff0000, v86
	v_pk_mul_f32 v[88:89], v[88:89], v[92:93]
	v_add_f32_e32 v92, 1.0, v101
	v_rcp_f32_e32 v101, v92
	v_pk_fma_f32 v[92:93], v[14:15], v[156:157], v[2:3]
	v_pk_fma_f32 v[86:87], v[24:25], v[152:153], v[142:143]
	v_pk_fma_f32 v[92:93], v[26:27], v[144:145], v[92:93]
	v_mul_f32_e32 v142, 0xbfb8aa3b, v86
	v_pk_fma_f32 v[92:93], v[30:31], v[102:103], v[92:93]
	v_rcp_f32_e32 v100, v100
	v_mul_f32_e32 v107, 0xbfb8aa3b, v92
; __device__ __forceinline__ unsigned pk2(float lo, float hi) { return f2bf(lo) | (f2bf(hi) << 16); }
; __device__ __forceinline__ float bflo(unsigned w) { return __uint_as_float(w << 16); }
; __device__ __forceinline__ float bfhi(unsigned w) { return __uint_as_float(w & 0xffff0000u); }
; __device__ __forceinline__ float sigmoidf_(float x) { return frcp_(1.0f + fexp_(-x)); }
; __device__ __forceinline__ void p3_conv(const Args& a, const Frame& F) {
;     ...
;     for (int item = F.bid * 4 + sub; item < TA / 16; item += F.G * 4) {
;         const int r0 = item * 16;
;         const int len = (r0 < T) ? SEQ : CTXL, pos0 = (r0 < T) ? (r0 & (SEQ - 1)) : ((r0 - T) & (CTXL - 1));
;         u32x4 rw[18];
; #pragma unroll
;         for (int i = 0; i < 18; ++i) { const int pos = pos0 + i - 1; rw[i] = (pos >= 0 && pos < len) ? *(const u32x4*)(PQK + (size_t)(r0 + i - 1) * 1024 + c0) : z; }
; #pragma unroll
;         for (int i = 0; i < 16; ++i) {
;             const unsigned wm[4] = {rw[i].x, rw[i].y, rw[i].z, rw[i].w}, wc_[4] = {rw[i + 1].x, rw[i + 1].y, rw[i + 1].z, rw[i + 1].w}, wp[4] = {rw[i + 2].x, rw[i + 2].y, rw[i + 2].z, rw[i + 2].w};
;             float o[8];
; #pragma unroll
;             for (int j = 0; j < 4; ++j) {
;                 const float a0 = bb[2 * j] + bflo(wm[j]) * w0[2 * j] + bflo(wc_[j]) * w1[2 * j] + bflo(wp[j]) * w2[2 * j];
;                 const float a1 = bb[2 * j + 1] + bfhi(wm[j]) * w0[2 * j + 1] + bfhi(wc_[j]) * w1[2 * j + 1] + bfhi(wp[j]) * w2[2 * j + 1];
;                 o[2 * j] = a0 * sigmoidf_(a0) * scl; o[2 * j + 1] = a1 * sigmoidf_(a1) * scl; }
;             u32x4 w; w.x = pk2(o[0], o[1]); w.y = pk2(o[2], o[3]); w.z = pk2(o[4], o[5]); w.w = pk2(o[6], o[7]);
;             *(u32x4*)(QKC + (size_t)(r0 + i) * 1024 + c0) = w;
	v_exp_f32_e32 v107, v107
	v_exp_f32_e32 v142, v142
	v_pk_mul_f32 v[84:85], v[84:85], v[100:101]
	v_pk_mul_f32 v[88:89], v[104:105], v[88:89]
	v_add_f32_e32 v100, 1.0, v107
	v_add_f32_e32 v101, 1.0, v142
	v_mul_f32_e32 v107, 0xbfb8aa3b, v93
	v_mul_f32_e32 v142, 0xbfb8aa3b, v87
	v_exp_f32_e32 v107, v107
	v_exp_f32_e32 v143, v142
	v_rcp_f32_e32 v142, v101
	v_rcp_f32_e32 v100, v100
	v_add_f32_e32 v101, 1.0, v107
	v_add_f32_e32 v107, 1.0, v143
	v_rcp_f32_e32 v143, v107
	v_rcp_f32_e32 v101, v101
	v_pk_mul_f32 v[84:85], v[104:105], v[84:85]
	v_add_u32_e32 v1, s11, v1
	v_pk_mul_f32 v[86:87], v[86:87], v[142:143]
	v_pk_mul_f32 v[92:93], v[92:93], v[100:101]
	v_pk_mul_f32 v[86:87], v[104:105], v[86:87]
	v_pk_mul_f32 v[92:93], v[104:105], v[92:93]
	v_bfe_u32 v100, v87, 16, 1
	v_bfe_u32 v101, v86, 16, 1
	v_bfe_u32 v107, v85, 16, 1
	v_bfe_u32 v142, v84, 16, 1
	v_add3_u32 v86, v86, v101, s14
	v_add3_u32 v87, v87, v100, s14
	v_bfe_u32 v100, v88, 16, 1
	v_bfe_u32 v101, v89, 16, 1
	v_add3_u32 v84, v84, v142, s14
	v_add3_u32 v85, v85, v107, s14
	v_bfe_u32 v107, v92, 16, 1
	v_bfe_u32 v142, v93, 16, 1
	v_add3_u32 v89, v89, v101, s14
	v_add3_u32 v88, v88, v100, s14
	v_add3_u32 v93, v93, v142, s14
	v_add3_u32 v92, v92, v107, s14
	v_lshrrev_b32_e32 v88, 16, v88
	v_lshrrev_b32_e32 v89, 16, v89
	v_lshrrev_b32_e32 v92, 16, v92
	v_lshrrev_b32_e32 v93, 16, v93
	v_and_or_b32 v85, v85, s13, v89
	v_and_or_b32 v84, v84, s13, v88
	v_lshlrev_b64 v[88:89], 11, v[140:141]
	v_and_or_b32 v87, v87, s13, v93
	v_and_or_b32 v86, v86, s13, v92
	v_lshl_add_u64 v[88:89], v[110:111], 0, v[88:89]
	global_store_dwordx4 v[88:89], v[84:87], off
	v_and_b32_e32 v93, 0xffff0000, v81
	v_and_b32_e32 v92, 0xffff0000, v80
	v_pk_fma_f32 v[84:85], v[10:11], v[94:95], v[6:7]
	v_lshlrev_b32_e32 v87, 16, v81
	v_pk_fma_f32 v[84:85], v[18:19], v[90:91], v[84:85]
	v_lshlrev_b32_e32 v86, 16, v80
	v_pk_fma_f32 v[84:85], v[22:23], v[86:87], v[84:85]
	v_and_b32_e32 v141, 0xffff0000, v83
	v_mul_f32_e32 v88, 0xbfb8aa3b, v84
	v_exp_f32_e32 v94, v88
	v_pk_fma_f32 v[88:89], v[114:115], v[98:99], v[112:113]
	v_lshlrev_b32_e32 v99, 16, v83
	v_pk_fma_f32 v[88:89], v[4:5], v[96:97], v[88:89]
	v_lshlrev_b32_e32 v98, 16, v82
	v_pk_fma_f32 v[80:81], v[16:17], v[92:93], v[88:89]
	v_and_b32_e32 v140, 0xffff0000, v82
	v_mul_f32_e32 v88, 0xbfb8aa3b, v80
	v_exp_f32_e32 v89, v88
	v_mul_f32_e32 v88, 0xbfb8aa3b, v85
	v_exp_f32_e32 v95, v88
	v_add_f32_e32 v88, 1.0, v94
	v_add_f32_e32 v94, 1.0, v89
	v_rcp_f32_e32 v88, v88
	v_add_f32_e32 v89, 1.0, v95
	v_mul_f32_e32 v95, 0xbfb8aa3b, v81
	v_rcp_f32_e32 v89, v89
	v_exp_f32_e32 v95, v95
	v_rcp_f32_e32 v94, v94
	v_lshlrev_b64 v[28:29], 11, v[28:29]
	v_pk_mul_f32 v[84:85], v[84:85], v[88:89]
	v_add_f32_e32 v88, 1.0, v95
	v_rcp_f32_e32 v95, v88
	v_pk_fma_f32 v[88:89], v[14:15], v[144:145], v[2:3]
	v_pk_mul_f32 v[84:85], v[104:105], v[84:85]
	v_pk_fma_f32 v[88:89], v[26:27], v[102:103], v[88:89]
	v_pk_mul_f32 v[80:81], v[80:81], v[94:95]
	v_pk_fma_f32 v[88:89], v[30:31], v[98:99], v[88:89]
	v_pk_mul_f32 v[80:81], v[104:105], v[80:81]
	v_mul_f32_e32 v100, 0xbfb8aa3b, v88
	v_exp_f32_e32 v107, v100
	v_pk_fma_f32 v[100:101], v[12:13], v[150:151], v[8:9]
	v_cmp_gt_i32_e32 vcc, 0, v1
	v_pk_fma_f32 v[100:101], v[20:21], v[152:153], v[100:101]
	v_add_f32_e32 v94, 1.0, v107
	v_pk_fma_f32 v[82:83], v[24:25], v[140:141], v[100:101]
	v_rcp_f32_e32 v94, v94
	v_mul_f32_e32 v100, 0xbfb8aa3b, v82
	v_exp_f32_e32 v100, v100
	v_lshl_add_u64 v[28:29], v[110:111], 0, v[28:29]
	s_or_b64 s[6:7], vcc, s[6:7]
	v_add_u32_e32 v106, s12, v106
	v_add_f32_e32 v95, 1.0, v100
	v_mul_f32_e32 v100, 0xbfb8aa3b, v89
	v_exp_f32_e32 v101, v100
	v_mul_f32_e32 v100, 0xbfb8aa3b, v83
	v_exp_f32_e32 v107, v100
	v_rcp_f32_e32 v100, v95
	v_add_f32_e32 v95, 1.0, v101
	v_rcp_f32_e32 v95, v95
	v_add_f32_e32 v101, 1.0, v107
	v_rcp_f32_e32 v101, v101
	v_pk_mul_f32 v[88:89], v[88:89], v[94:95]
	s_nop 0
	v_pk_mul_f32 v[88:89], v[104:105], v[88:89]
	v_pk_mul_f32 v[82:83], v[82:83], v[100:101]
	v_bfe_u32 v100, v81, 16, 1
	v_pk_mul_f32 v[82:83], v[104:105], v[82:83]
	v_bfe_u32 v101, v80, 16, 1
	v_bfe_u32 v94, v83, 16, 1
	v_bfe_u32 v95, v82, 16, 1
	v_add3_u32 v82, v82, v95, s14
	v_add3_u32 v83, v83, v94, s14
	v_bfe_u32 v94, v84, 16, 1
	v_bfe_u32 v95, v85, 16, 1
	v_add3_u32 v80, v80, v101, s14
	v_add3_u32 v81, v81, v100, s14
	v_bfe_u32 v100, v88, 16, 1
	v_bfe_u32 v101, v89, 16, 1
	v_add3_u32 v85, v85, v95, s14
	v_add3_u32 v84, v84, v94, s14
	v_add3_u32 v89, v89, v101, s14
	v_add3_u32 v88, v88, v100, s14
	v_lshrrev_b32_e32 v84, 16, v84
	v_lshrrev_b32_e32 v85, 16, v85
	v_lshrrev_b32_e32 v88, 16, v88
	v_lshrrev_b32_e32 v89, 16, v89
	v_and_or_b32 v81, v81, s13, v85
	v_and_or_b32 v80, v80, s13, v84
	v_lshlrev_b64 v[84:85], 11, v[138:139]
	v_and_or_b32 v83, v83, s13, v89
	v_and_or_b32 v82, v82, s13, v88
	v_lshl_add_u64 v[84:85], v[110:111], 0, v[84:85]
	global_store_dwordx4 v[84:85], v[80:83], off
	v_and_b32_e32 v89, 0xffff0000, v77
	v_and_b32_e32 v88, 0xffff0000, v76
	v_pk_fma_f32 v[80:81], v[10:11], v[90:91], v[6:7]
	v_lshlrev_b32_e32 v83, 16, v77
	v_pk_fma_f32 v[80:81], v[18:19], v[86:87], v[80:81]
	v_lshlrev_b32_e32 v82, 16, v76
	v_pk_fma_f32 v[80:81], v[22:23], v[82:83], v[80:81]
	v_lshlrev_b32_e32 v95, 16, v79
	v_mul_f32_e32 v84, 0xbfb8aa3b, v80
	v_exp_f32_e32 v90, v84
	v_pk_fma_f32 v[84:85], v[114:115], v[96:97], v[112:113]
	v_lshlrev_b32_e32 v94, 16, v78
	v_pk_fma_f32 v[84:85], v[4:5], v[92:93], v[84:85]
	v_and_b32_e32 v101, 0xffff0000, v79
	v_pk_fma_f32 v[76:77], v[16:17], v[88:89], v[84:85]
	v_and_b32_e32 v100, 0xffff0000, v78
	v_mul_f32_e32 v84, 0xbfb8aa3b, v76
	v_exp_f32_e32 v85, v84
	v_mul_f32_e32 v84, 0xbfb8aa3b, v81
; __device__ __forceinline__ unsigned pk2(float lo, float hi) { return f2bf(lo) | (f2bf(hi) << 16); }
; __device__ __forceinline__ float bflo(unsigned w) { return __uint_as_float(w << 16); }
; __device__ __forceinline__ float bfhi(unsigned w) { return __uint_as_float(w & 0xffff0000u); }
; __device__ __forceinline__ float sigmoidf_(float x) { return frcp_(1.0f + fexp_(-x)); }
; __device__ __forceinline__ void p3_conv(const Args& a, const Frame& F) {
;     ...
;         for (int i = 0; i < 16; ++i) {
;             const unsigned wm[4] = {rw[i].x, rw[i].y, rw[i].z, rw[i].w}, wc_[4] = {rw[i + 1].x, rw[i + 1].y, rw[i + 1].z, rw[i + 1].w}, wp[4] = {rw[i + 2].x, rw[i + 2].y, rw[i + 2].z, rw[i + 2].w};
;             float o[8];
; #pragma unroll
;             for (int j = 0; j < 4; ++j) {
;                 const float a0 = bb[2 * j] + bflo(wm[j]) * w0[2 * j] + bflo(wc_[j]) * w1[2 * j] + bflo(wp[j]) * w2[2 * j];
;                 const float a1 = bb[2 * j + 1] + bfhi(wm[j]) * w0[2 * j + 1] + bfhi(wc_[j]) * w1[2 * j + 1] + bfhi(wp[j]) * w2[2 * j + 1];
;                 o[2 * j] = a0 * sigmoidf_(a0) * scl; o[2 * j + 1] = a1 * sigmoidf_(a1) * scl; }
;             u32x4 w; w.x = pk2(o[0], o[1]); w.y = pk2(o[2], o[3]); w.z = pk2(o[4], o[5]); w.w = pk2(o[6], o[7]);
;             *(u32x4*)(QKC + (size_t)(r0 + i) * 1024 + c0) = w;
	v_exp_f32_e32 v91, v84
	v_add_f32_e32 v84, 1.0, v90
	v_add_f32_e32 v90, 1.0, v85
	v_rcp_f32_e32 v84, v84
	v_add_f32_e32 v85, 1.0, v91
	v_mul_f32_e32 v91, 0xbfb8aa3b, v77
	v_rcp_f32_e32 v85, v85
	v_exp_f32_e32 v91, v91
	v_rcp_f32_e32 v90, v90
	v_pk_mul_f32 v[80:81], v[80:81], v[84:85]
	v_add_f32_e32 v84, 1.0, v91
	v_rcp_f32_e32 v91, v84
	v_pk_fma_f32 v[84:85], v[14:15], v[102:103], v[2:3]
	v_pk_mul_f32 v[80:81], v[104:105], v[80:81]
	v_pk_fma_f32 v[84:85], v[26:27], v[98:99], v[84:85]
	v_pk_mul_f32 v[76:77], v[76:77], v[90:91]
	v_pk_fma_f32 v[84:85], v[30:31], v[94:95], v[84:85]
	v_pk_mul_f32 v[76:77], v[104:105], v[76:77]
	v_mul_f32_e32 v96, 0xbfb8aa3b, v84
	v_exp_f32_e32 v102, v96
	v_pk_fma_f32 v[96:97], v[12:13], v[152:153], v[8:9]
	v_add_f32_e32 v90, 1.0, v102
	v_pk_fma_f32 v[96:97], v[20:21], v[140:141], v[96:97]
	v_rcp_f32_e32 v90, v90
	v_pk_fma_f32 v[78:79], v[24:25], v[100:101], v[96:97]
	s_nop 0
	v_mul_f32_e32 v96, 0xbfb8aa3b, v78
	v_exp_f32_e32 v96, v96
	s_nop 0
	v_add_f32_e32 v91, 1.0, v96
	v_mul_f32_e32 v96, 0xbfb8aa3b, v85
	v_exp_f32_e32 v97, v96
	v_mul_f32_e32 v96, 0xbfb8aa3b, v79
	v_exp_f32_e32 v102, v96
	v_rcp_f32_e32 v96, v91
	v_add_f32_e32 v91, 1.0, v97
	v_rcp_f32_e32 v91, v91
	v_add_f32_e32 v97, 1.0, v102
	v_rcp_f32_e32 v97, v97
	v_pk_mul_f32 v[84:85], v[84:85], v[90:91]
	s_nop 0
	v_pk_mul_f32 v[84:85], v[104:105], v[84:85]
	v_pk_mul_f32 v[78:79], v[78:79], v[96:97]
	v_bfe_u32 v96, v77, 16, 1
	v_pk_mul_f32 v[78:79], v[104:105], v[78:79]
	v_bfe_u32 v97, v76, 16, 1
	v_bfe_u32 v90, v79, 16, 1
	v_bfe_u32 v91, v78, 16, 1
	v_add3_u32 v78, v78, v91, s14
	v_add3_u32 v79, v79, v90, s14
	v_bfe_u32 v90, v80, 16, 1
	v_bfe_u32 v91, v81, 16, 1
	v_add3_u32 v76, v76, v97, s14
	v_add3_u32 v77, v77, v96, s14
	v_bfe_u32 v96, v84, 16, 1
	v_bfe_u32 v97, v85, 16, 1
	v_add3_u32 v81, v81, v91, s14
	v_add3_u32 v80, v80, v90, s14
	v_add3_u32 v85, v85, v97, s14
	v_add3_u32 v84, v84, v96, s14
	v_lshrrev_b32_e32 v80, 16, v80
	v_lshrrev_b32_e32 v81, 16, v81
	v_lshrrev_b32_e32 v84, 16, v84
	v_lshrrev_b32_e32 v85, 16, v85
	v_and_or_b32 v77, v77, s13, v81
	v_and_or_b32 v76, v76, s13, v80
	v_lshlrev_b64 v[80:81], 11, v[136:137]
	v_and_or_b32 v79, v79, s13, v85
	v_and_or_b32 v78, v78, s13, v84
	v_lshl_add_u64 v[80:81], v[110:111], 0, v[80:81]
	global_store_dwordx4 v[80:81], v[76:79], off
	v_and_b32_e32 v85, 0xffff0000, v73
	v_and_b32_e32 v84, 0xffff0000, v72
	v_pk_fma_f32 v[76:77], v[10:11], v[86:87], v[6:7]
	v_lshlrev_b32_e32 v79, 16, v73
	v_pk_fma_f32 v[76:77], v[18:19], v[82:83], v[76:77]
	v_lshlrev_b32_e32 v78, 16, v72
	v_pk_fma_f32 v[76:77], v[22:23], v[78:79], v[76:77]
	v_lshlrev_b32_e32 v91, 16, v75
	v_mul_f32_e32 v80, 0xbfb8aa3b, v76
	v_exp_f32_e32 v86, v80
	v_pk_fma_f32 v[80:81], v[114:115], v[92:93], v[112:113]
	v_lshlrev_b32_e32 v90, 16, v74
	v_pk_fma_f32 v[80:81], v[4:5], v[88:89], v[80:81]
	v_and_b32_e32 v97, 0xffff0000, v75
	v_pk_fma_f32 v[72:73], v[16:17], v[84:85], v[80:81]
	v_and_b32_e32 v96, 0xffff0000, v74
	v_mul_f32_e32 v80, 0xbfb8aa3b, v72
	v_exp_f32_e32 v81, v80
	v_mul_f32_e32 v80, 0xbfb8aa3b, v77
	v_exp_f32_e32 v87, v80
	v_add_f32_e32 v80, 1.0, v86
	v_add_f32_e32 v86, 1.0, v81
	v_rcp_f32_e32 v80, v80
	v_add_f32_e32 v81, 1.0, v87
	v_mul_f32_e32 v87, 0xbfb8aa3b, v73
	v_rcp_f32_e32 v81, v81
	v_exp_f32_e32 v87, v87
	v_rcp_f32_e32 v86, v86
	v_pk_mul_f32 v[76:77], v[76:77], v[80:81]
	v_add_f32_e32 v80, 1.0, v87
	v_rcp_f32_e32 v87, v80
	v_pk_fma_f32 v[80:81], v[14:15], v[98:99], v[2:3]
	v_pk_mul_f32 v[76:77], v[104:105], v[76:77]
	v_pk_fma_f32 v[80:81], v[26:27], v[94:95], v[80:81]
	v_pk_mul_f32 v[72:73], v[72:73], v[86:87]
	v_pk_fma_f32 v[80:81], v[30:31], v[90:91], v[80:81]
	v_pk_mul_f32 v[72:73], v[104:105], v[72:73]
	v_mul_f32_e32 v92, 0xbfb8aa3b, v80
	v_exp_f32_e32 v98, v92
	v_pk_fma_f32 v[92:93], v[12:13], v[140:141], v[8:9]
	v_add_f32_e32 v86, 1.0, v98
	v_pk_fma_f32 v[92:93], v[20:21], v[100:101], v[92:93]
	v_rcp_f32_e32 v86, v86
	v_pk_fma_f32 v[74:75], v[24:25], v[96:97], v[92:93]
	s_nop 0
	v_mul_f32_e32 v92, 0xbfb8aa3b, v74
	v_exp_f32_e32 v92, v92
	s_nop 0
	v_add_f32_e32 v87, 1.0, v92
	v_mul_f32_e32 v92, 0xbfb8aa3b, v81
	v_exp_f32_e32 v93, v92
	v_mul_f32_e32 v92, 0xbfb8aa3b, v75
	v_exp_f32_e32 v98, v92
	v_rcp_f32_e32 v92, v87
	v_add_f32_e32 v87, 1.0, v93
	v_rcp_f32_e32 v87, v87
	v_add_f32_e32 v93, 1.0, v98
	v_rcp_f32_e32 v93, v93
	v_pk_mul_f32 v[80:81], v[80:81], v[86:87]
	s_nop 0
	v_pk_mul_f32 v[80:81], v[104:105], v[80:81]
	v_pk_mul_f32 v[74:75], v[74:75], v[92:93]
	v_bfe_u32 v92, v73, 16, 1
	v_pk_mul_f32 v[74:75], v[104:105], v[74:75]
	v_bfe_u32 v93, v72, 16, 1
	v_bfe_u32 v86, v75, 16, 1
	v_bfe_u32 v87, v74, 16, 1
	v_add3_u32 v74, v74, v87, s14
	v_add3_u32 v75, v75, v86, s14
	v_bfe_u32 v86, v76, 16, 1
	v_bfe_u32 v87, v77, 16, 1
	v_add3_u32 v72, v72, v93, s14
	v_add3_u32 v73, v73, v92, s14
	v_bfe_u32 v92, v80, 16, 1
	v_bfe_u32 v93, v81, 16, 1
	v_add3_u32 v77, v77, v87, s14
	v_add3_u32 v76, v76, v86, s14
	v_add3_u32 v81, v81, v93, s14
	v_add3_u32 v80, v80, v92, s14
	v_lshrrev_b32_e32 v76, 16, v76
	v_lshrrev_b32_e32 v77, 16, v77
	v_lshrrev_b32_e32 v80, 16, v80
	v_lshrrev_b32_e32 v81, 16, v81
	v_and_or_b32 v73, v73, s13, v77
	v_and_or_b32 v72, v72, s13, v76
	v_lshlrev_b64 v[76:77], 11, v[134:135]
	v_and_or_b32 v75, v75, s13, v81
	v_and_or_b32 v74, v74, s13, v80
	v_lshl_add_u64 v[76:77], v[110:111], 0, v[76:77]
	global_store_dwordx4 v[76:77], v[72:75], off
	v_and_b32_e32 v81, 0xffff0000, v69
	v_and_b32_e32 v80, 0xffff0000, v68
	v_pk_fma_f32 v[72:73], v[10:11], v[82:83], v[6:7]
	v_lshlrev_b32_e32 v75, 16, v69
	v_pk_fma_f32 v[72:73], v[18:19], v[78:79], v[72:73]
	v_lshlrev_b32_e32 v74, 16, v68
	v_pk_fma_f32 v[72:73], v[22:23], v[74:75], v[72:73]
; __device__ __forceinline__ unsigned pk2(float lo, float hi) { return f2bf(lo) | (f2bf(hi) << 16); }
; __device__ __forceinline__ float bflo(unsigned w) { return __uint_as_float(w << 16); }
; __device__ __forceinline__ float bfhi(unsigned w) { return __uint_as_float(w & 0xffff0000u); }
; __device__ __forceinline__ float sigmoidf_(float x) { return frcp_(1.0f + fexp_(-x)); }
; __device__ __forceinline__ void p3_conv(const Args& a, const Frame& F) {
;     ...
;         for (int i = 0; i < 16; ++i) {
;             const unsigned wm[4] = {rw[i].x, rw[i].y, rw[i].z, rw[i].w}, wc_[4] = {rw[i + 1].x, rw[i + 1].y, rw[i + 1].z, rw[i + 1].w}, wp[4] = {rw[i + 2].x, rw[i + 2].y, rw[i + 2].z, rw[i + 2].w};
;             float o[8];
; #pragma unroll
;             for (int j = 0; j < 4; ++j) {
;                 const float a0 = bb[2 * j] + bflo(wm[j]) * w0[2 * j] + bflo(wc_[j]) * w1[2 * j] + bflo(wp[j]) * w2[2 * j];
;                 const float a1 = bb[2 * j + 1] + bfhi(wm[j]) * w0[2 * j + 1] + bfhi(wc_[j]) * w1[2 * j + 1] + bfhi(wp[j]) * w2[2 * j + 1];
;                 o[2 * j] = a0 * sigmoidf_(a0) * scl; o[2 * j + 1] = a1 * sigmoidf_(a1) * scl; }
;             u32x4 w; w.x = pk2(o[0], o[1]); w.y = pk2(o[2], o[3]); w.z = pk2(o[4], o[5]); w.w = pk2(o[6], o[7]);
;             *(u32x4*)(QKC + (size_t)(r0 + i) * 1024 + c0) = w;
	v_lshlrev_b32_e32 v87, 16, v71
	v_mul_f32_e32 v76, 0xbfb8aa3b, v72
	v_exp_f32_e32 v82, v76
	v_pk_fma_f32 v[76:77], v[114:115], v[88:89], v[112:113]
	v_lshlrev_b32_e32 v86, 16, v70
	v_pk_fma_f32 v[76:77], v[4:5], v[84:85], v[76:77]
	v_and_b32_e32 v93, 0xffff0000, v71
	v_pk_fma_f32 v[68:69], v[16:17], v[80:81], v[76:77]
	v_and_b32_e32 v92, 0xffff0000, v70
	v_mul_f32_e32 v76, 0xbfb8aa3b, v68
	v_exp_f32_e32 v77, v76
	v_mul_f32_e32 v76, 0xbfb8aa3b, v73
	v_exp_f32_e32 v83, v76
	v_add_f32_e32 v76, 1.0, v82
	v_add_f32_e32 v82, 1.0, v77
	v_rcp_f32_e32 v76, v76
	v_add_f32_e32 v77, 1.0, v83
	v_mul_f32_e32 v83, 0xbfb8aa3b, v69
	v_rcp_f32_e32 v77, v77
	v_exp_f32_e32 v83, v83
	v_rcp_f32_e32 v82, v82
	v_pk_mul_f32 v[72:73], v[72:73], v[76:77]
	v_add_f32_e32 v76, 1.0, v83
	v_rcp_f32_e32 v83, v76
	v_pk_fma_f32 v[76:77], v[14:15], v[94:95], v[2:3]
	v_pk_mul_f32 v[72:73], v[104:105], v[72:73]
	v_pk_fma_f32 v[76:77], v[26:27], v[90:91], v[76:77]
	v_pk_mul_f32 v[68:69], v[68:69], v[82:83]
	v_pk_fma_f32 v[76:77], v[30:31], v[86:87], v[76:77]
	v_pk_mul_f32 v[68:69], v[104:105], v[68:69]
	v_mul_f32_e32 v88, 0xbfb8aa3b, v76
	v_exp_f32_e32 v94, v88
	v_pk_fma_f32 v[88:89], v[12:13], v[100:101], v[8:9]
	v_add_f32_e32 v82, 1.0, v94
	v_pk_fma_f32 v[88:89], v[20:21], v[96:97], v[88:89]
	v_rcp_f32_e32 v82, v82
	v_pk_fma_f32 v[70:71], v[24:25], v[92:93], v[88:89]
	s_nop 0
	v_mul_f32_e32 v88, 0xbfb8aa3b, v70
	v_exp_f32_e32 v88, v88
	s_nop 0
	v_add_f32_e32 v83, 1.0, v88
	v_mul_f32_e32 v88, 0xbfb8aa3b, v77
	v_exp_f32_e32 v89, v88
	v_mul_f32_e32 v88, 0xbfb8aa3b, v71
	v_exp_f32_e32 v94, v88
	v_rcp_f32_e32 v88, v83
	v_add_f32_e32 v83, 1.0, v89
	v_rcp_f32_e32 v83, v83
	v_add_f32_e32 v89, 1.0, v94
	v_rcp_f32_e32 v89, v89
	v_pk_mul_f32 v[76:77], v[76:77], v[82:83]
	s_nop 0
	v_pk_mul_f32 v[76:77], v[104:105], v[76:77]
	v_pk_mul_f32 v[70:71], v[70:71], v[88:89]
	v_bfe_u32 v88, v69, 16, 1
	v_pk_mul_f32 v[70:71], v[104:105], v[70:71]
	v_bfe_u32 v89, v68, 16, 1
	v_bfe_u32 v82, v71, 16, 1
	v_bfe_u32 v83, v70, 16, 1
	v_add3_u32 v70, v70, v83, s14
	v_add3_u32 v71, v71, v82, s14
	v_bfe_u32 v82, v72, 16, 1
	v_bfe_u32 v83, v73, 16, 1
	v_add3_u32 v68, v68, v89, s14
	v_add3_u32 v69, v69, v88, s14
	v_bfe_u32 v88, v76, 16, 1
	v_bfe_u32 v89, v77, 16, 1
	v_add3_u32 v73, v73, v83, s14
	v_add3_u32 v72, v72, v82, s14
	v_add3_u32 v77, v77, v89, s14
	v_add3_u32 v76, v76, v88, s14
	v_lshrrev_b32_e32 v72, 16, v72
	v_lshrrev_b32_e32 v73, 16, v73
	v_lshrrev_b32_e32 v76, 16, v76
	v_lshrrev_b32_e32 v77, 16, v77
	v_and_or_b32 v69, v69, s13, v73
	v_and_or_b32 v68, v68, s13, v72
	v_lshlrev_b64 v[72:73], 11, v[132:133]
	v_and_or_b32 v71, v71, s13, v77
	v_and_or_b32 v70, v70, s13, v76
	v_lshl_add_u64 v[72:73], v[110:111], 0, v[72:73]
	global_store_dwordx4 v[72:73], v[68:71], off
	v_and_b32_e32 v77, 0xffff0000, v65
	v_and_b32_e32 v76, 0xffff0000, v64
	v_pk_fma_f32 v[68:69], v[10:11], v[78:79], v[6:7]
	v_lshlrev_b32_e32 v71, 16, v65
	v_pk_fma_f32 v[68:69], v[18:19], v[74:75], v[68:69]
	v_lshlrev_b32_e32 v70, 16, v64
	v_pk_fma_f32 v[68:69], v[22:23], v[70:71], v[68:69]
	v_lshlrev_b32_e32 v83, 16, v67
	v_mul_f32_e32 v72, 0xbfb8aa3b, v68
	v_exp_f32_e32 v78, v72
	v_pk_fma_f32 v[72:73], v[114:115], v[84:85], v[112:113]
	v_lshlrev_b32_e32 v82, 16, v66
	v_pk_fma_f32 v[72:73], v[4:5], v[80:81], v[72:73]
	v_and_b32_e32 v89, 0xffff0000, v67
	v_pk_fma_f32 v[64:65], v[16:17], v[76:77], v[72:73]
	v_and_b32_e32 v88, 0xffff0000, v66
	v_mul_f32_e32 v72, 0xbfb8aa3b, v64
	v_exp_f32_e32 v73, v72
	v_mul_f32_e32 v72, 0xbfb8aa3b, v69
	v_exp_f32_e32 v79, v72
	v_add_f32_e32 v72, 1.0, v78
	v_add_f32_e32 v78, 1.0, v73
	v_rcp_f32_e32 v72, v72
	v_add_f32_e32 v73, 1.0, v79
	v_mul_f32_e32 v79, 0xbfb8aa3b, v65
	v_rcp_f32_e32 v73, v73
	v_exp_f32_e32 v79, v79
	v_rcp_f32_e32 v78, v78
	v_pk_mul_f32 v[68:69], v[68:69], v[72:73]
	v_add_f32_e32 v72, 1.0, v79
	v_rcp_f32_e32 v79, v72
	v_pk_fma_f32 v[72:73], v[14:15], v[90:91], v[2:3]
	v_pk_mul_f32 v[68:69], v[104:105], v[68:69]
	v_pk_fma_f32 v[72:73], v[26:27], v[86:87], v[72:73]
	v_pk_mul_f32 v[64:65], v[64:65], v[78:79]
	v_pk_fma_f32 v[72:73], v[30:31], v[82:83], v[72:73]
	v_pk_mul_f32 v[64:65], v[104:105], v[64:65]
	v_mul_f32_e32 v84, 0xbfb8aa3b, v72
	v_exp_f32_e32 v90, v84
	v_pk_fma_f32 v[84:85], v[12:13], v[96:97], v[8:9]
	v_add_f32_e32 v78, 1.0, v90
	v_pk_fma_f32 v[84:85], v[20:21], v[92:93], v[84:85]
	v_rcp_f32_e32 v78, v78
	v_pk_fma_f32 v[66:67], v[24:25], v[88:89], v[84:85]
	s_nop 0
	v_mul_f32_e32 v84, 0xbfb8aa3b, v66
	v_exp_f32_e32 v84, v84
	s_nop 0
	v_add_f32_e32 v79, 1.0, v84
	v_mul_f32_e32 v84, 0xbfb8aa3b, v73
	v_exp_f32_e32 v85, v84
	v_mul_f32_e32 v84, 0xbfb8aa3b, v67
	v_exp_f32_e32 v90, v84
	v_rcp_f32_e32 v84, v79
	v_add_f32_e32 v79, 1.0, v85
	v_rcp_f32_e32 v79, v79
	v_add_f32_e32 v85, 1.0, v90
	v_rcp_f32_e32 v85, v85
	v_pk_mul_f32 v[72:73], v[72:73], v[78:79]
	s_nop 0
	v_pk_mul_f32 v[72:73], v[104:105], v[72:73]
	v_pk_mul_f32 v[66:67], v[66:67], v[84:85]
	v_bfe_u32 v84, v65, 16, 1
	v_pk_mul_f32 v[66:67], v[104:105], v[66:67]
	v_bfe_u32 v85, v64, 16, 1
	v_bfe_u32 v78, v67, 16, 1
	v_bfe_u32 v79, v66, 16, 1
	v_add3_u32 v66, v66, v79, s14
	v_add3_u32 v67, v67, v78, s14
	v_bfe_u32 v78, v68, 16, 1
	v_bfe_u32 v79, v69, 16, 1
	v_add3_u32 v64, v64, v85, s14
	v_add3_u32 v65, v65, v84, s14
	v_bfe_u32 v84, v72, 16, 1
	v_bfe_u32 v85, v73, 16, 1
	v_add3_u32 v69, v69, v79, s14
	v_add3_u32 v68, v68, v78, s14
	v_add3_u32 v73, v73, v85, s14
	v_add3_u32 v72, v72, v84, s14
	v_lshrrev_b32_e32 v68, 16, v68
	v_lshrrev_b32_e32 v69, 16, v69
	v_lshrrev_b32_e32 v72, 16, v72
	v_lshrrev_b32_e32 v73, 16, v73
	v_and_or_b32 v65, v65, s13, v69
	v_and_or_b32 v64, v64, s13, v68
	v_lshlrev_b64 v[68:69], 11, v[130:131]
; __device__ __forceinline__ unsigned pk2(float lo, float hi) { return f2bf(lo) | (f2bf(hi) << 16); }
; __device__ __forceinline__ float bflo(unsigned w) { return __uint_as_float(w << 16); }
; __device__ __forceinline__ float bfhi(unsigned w) { return __uint_as_float(w & 0xffff0000u); }
; __device__ __forceinline__ float sigmoidf_(float x) { return frcp_(1.0f + fexp_(-x)); }
; __device__ __forceinline__ void p3_conv(const Args& a, const Frame& F) {
;     ...
;         for (int i = 0; i < 16; ++i) {
;             const unsigned wm[4] = {rw[i].x, rw[i].y, rw[i].z, rw[i].w}, wc_[4] = {rw[i + 1].x, rw[i + 1].y, rw[i + 1].z, rw[i + 1].w}, wp[4] = {rw[i + 2].x, rw[i + 2].y, rw[i + 2].z, rw[i + 2].w};
;             float o[8];
; #pragma unroll
;             for (int j = 0; j < 4; ++j) {
;                 const float a0 = bb[2 * j] + bflo(wm[j]) * w0[2 * j] + bflo(wc_[j]) * w1[2 * j] + bflo(wp[j]) * w2[2 * j];
;                 const float a1 = bb[2 * j + 1] + bfhi(wm[j]) * w0[2 * j + 1] + bfhi(wc_[j]) * w1[2 * j + 1] + bfhi(wp[j]) * w2[2 * j + 1];
;                 o[2 * j] = a0 * sigmoidf_(a0) * scl; o[2 * j + 1] = a1 * sigmoidf_(a1) * scl; }
;             u32x4 w; w.x = pk2(o[0], o[1]); w.y = pk2(o[2], o[3]); w.z = pk2(o[4], o[5]); w.w = pk2(o[6], o[7]);
;             *(u32x4*)(QKC + (size_t)(r0 + i) * 1024 + c0) = w;
	v_and_or_b32 v67, v67, s13, v73
	v_and_or_b32 v66, v66, s13, v72
	v_lshl_add_u64 v[68:69], v[110:111], 0, v[68:69]
	global_store_dwordx4 v[68:69], v[64:67], off
	v_and_b32_e32 v73, 0xffff0000, v61
	v_and_b32_e32 v72, 0xffff0000, v60
	v_pk_fma_f32 v[64:65], v[10:11], v[74:75], v[6:7]
	v_lshlrev_b32_e32 v67, 16, v61
	v_pk_fma_f32 v[64:65], v[18:19], v[70:71], v[64:65]
	v_lshlrev_b32_e32 v66, 16, v60
	v_pk_fma_f32 v[64:65], v[22:23], v[66:67], v[64:65]
	v_lshlrev_b32_e32 v79, 16, v63
	v_mul_f32_e32 v68, 0xbfb8aa3b, v64
	v_exp_f32_e32 v74, v68
	v_pk_fma_f32 v[68:69], v[114:115], v[80:81], v[112:113]
	v_lshlrev_b32_e32 v78, 16, v62
	v_pk_fma_f32 v[68:69], v[4:5], v[76:77], v[68:69]
	v_and_b32_e32 v85, 0xffff0000, v63
	v_pk_fma_f32 v[60:61], v[16:17], v[72:73], v[68:69]
	v_and_b32_e32 v84, 0xffff0000, v62
	v_mul_f32_e32 v68, 0xbfb8aa3b, v60
	v_exp_f32_e32 v69, v68
	v_mul_f32_e32 v68, 0xbfb8aa3b, v65
	v_exp_f32_e32 v75, v68
	v_add_f32_e32 v68, 1.0, v74
	v_add_f32_e32 v74, 1.0, v69
	v_rcp_f32_e32 v68, v68
	v_add_f32_e32 v69, 1.0, v75
	v_mul_f32_e32 v75, 0xbfb8aa3b, v61
	v_rcp_f32_e32 v69, v69
	v_exp_f32_e32 v75, v75
	v_rcp_f32_e32 v74, v74
	v_pk_mul_f32 v[64:65], v[64:65], v[68:69]
	v_add_f32_e32 v68, 1.0, v75
	v_rcp_f32_e32 v75, v68
	v_pk_fma_f32 v[68:69], v[14:15], v[86:87], v[2:3]
	v_pk_mul_f32 v[64:65], v[104:105], v[64:65]
	v_pk_fma_f32 v[68:69], v[26:27], v[82:83], v[68:69]
	v_pk_mul_f32 v[60:61], v[60:61], v[74:75]
	v_pk_fma_f32 v[68:69], v[30:31], v[78:79], v[68:69]
	v_pk_mul_f32 v[60:61], v[104:105], v[60:61]
	v_mul_f32_e32 v80, 0xbfb8aa3b, v68
	v_exp_f32_e32 v86, v80
	v_pk_fma_f32 v[80:81], v[12:13], v[92:93], v[8:9]
	v_add_f32_e32 v74, 1.0, v86
	v_pk_fma_f32 v[80:81], v[20:21], v[88:89], v[80:81]
	v_rcp_f32_e32 v74, v74
	v_pk_fma_f32 v[62:63], v[24:25], v[84:85], v[80:81]
	s_nop 0
	v_mul_f32_e32 v80, 0xbfb8aa3b, v62
	v_exp_f32_e32 v80, v80
	s_nop 0
	v_add_f32_e32 v75, 1.0, v80
	v_mul_f32_e32 v80, 0xbfb8aa3b, v69
	v_exp_f32_e32 v81, v80
	v_mul_f32_e32 v80, 0xbfb8aa3b, v63
	v_exp_f32_e32 v86, v80
	v_rcp_f32_e32 v80, v75
	v_add_f32_e32 v75, 1.0, v81
	v_rcp_f32_e32 v75, v75
	v_add_f32_e32 v81, 1.0, v86
	v_rcp_f32_e32 v81, v81
	v_pk_mul_f32 v[68:69], v[68:69], v[74:75]
	s_nop 0
	v_pk_mul_f32 v[68:69], v[104:105], v[68:69]
	v_pk_mul_f32 v[62:63], v[62:63], v[80:81]
	v_bfe_u32 v80, v61, 16, 1
	v_pk_mul_f32 v[62:63], v[104:105], v[62:63]
	v_bfe_u32 v81, v60, 16, 1
	v_bfe_u32 v74, v63, 16, 1
	v_bfe_u32 v75, v62, 16, 1
	v_add3_u32 v62, v62, v75, s14
	v_add3_u32 v63, v63, v74, s14
	v_bfe_u32 v74, v64, 16, 1
	v_bfe_u32 v75, v65, 16, 1
	v_add3_u32 v60, v60, v81, s14
	v_add3_u32 v61, v61, v80, s14
	v_bfe_u32 v80, v68, 16, 1
	v_bfe_u32 v81, v69, 16, 1
	v_add3_u32 v65, v65, v75, s14
	v_add3_u32 v64, v64, v74, s14
	v_add3_u32 v69, v69, v81, s14
	v_add3_u32 v68, v68, v80, s14
	v_lshrrev_b32_e32 v64, 16, v64
	v_lshrrev_b32_e32 v65, 16, v65
	v_lshrrev_b32_e32 v68, 16, v68
	v_lshrrev_b32_e32 v69, 16, v69
	v_and_or_b32 v61, v61, s13, v65
	v_and_or_b32 v60, v60, s13, v64
	v_lshlrev_b64 v[64:65], 11, v[128:129]
	v_and_or_b32 v63, v63, s13, v69
	v_and_or_b32 v62, v62, s13, v68
	v_lshl_add_u64 v[64:65], v[110:111], 0, v[64:65]
	global_store_dwordx4 v[64:65], v[60:63], off
	v_and_b32_e32 v69, 0xffff0000, v57
	v_and_b32_e32 v68, 0xffff0000, v56
	v_pk_fma_f32 v[60:61], v[10:11], v[70:71], v[6:7]
	v_lshlrev_b32_e32 v63, 16, v57
	v_pk_fma_f32 v[60:61], v[18:19], v[66:67], v[60:61]
	v_lshlrev_b32_e32 v62, 16, v56
	v_pk_fma_f32 v[60:61], v[22:23], v[62:63], v[60:61]
	v_lshlrev_b32_e32 v75, 16, v59
	v_mul_f32_e32 v64, 0xbfb8aa3b, v60
	v_exp_f32_e32 v70, v64
	v_pk_fma_f32 v[64:65], v[114:115], v[76:77], v[112:113]
	v_lshlrev_b32_e32 v74, 16, v58
	v_pk_fma_f32 v[64:65], v[4:5], v[72:73], v[64:65]
	v_and_b32_e32 v81, 0xffff0000, v59
	v_pk_fma_f32 v[56:57], v[16:17], v[68:69], v[64:65]
	v_and_b32_e32 v80, 0xffff0000, v58
	v_mul_f32_e32 v64, 0xbfb8aa3b, v56
	v_exp_f32_e32 v65, v64
	v_mul_f32_e32 v64, 0xbfb8aa3b, v61
	v_exp_f32_e32 v71, v64
	v_add_f32_e32 v64, 1.0, v70
	v_add_f32_e32 v70, 1.0, v65
	v_rcp_f32_e32 v64, v64
	v_add_f32_e32 v65, 1.0, v71
	v_mul_f32_e32 v71, 0xbfb8aa3b, v57
	v_rcp_f32_e32 v65, v65
	v_exp_f32_e32 v71, v71
	v_rcp_f32_e32 v70, v70
	v_pk_mul_f32 v[60:61], v[60:61], v[64:65]
	v_add_f32_e32 v64, 1.0, v71
	v_rcp_f32_e32 v71, v64
	v_pk_fma_f32 v[64:65], v[14:15], v[82:83], v[2:3]
	v_pk_mul_f32 v[60:61], v[104:105], v[60:61]
	v_pk_fma_f32 v[64:65], v[26:27], v[78:79], v[64:65]
	v_pk_mul_f32 v[56:57], v[56:57], v[70:71]
	v_pk_fma_f32 v[64:65], v[30:31], v[74:75], v[64:65]
	v_pk_mul_f32 v[56:57], v[104:105], v[56:57]
	v_mul_f32_e32 v76, 0xbfb8aa3b, v64
	v_exp_f32_e32 v82, v76
	v_pk_fma_f32 v[76:77], v[12:13], v[88:89], v[8:9]
	v_add_f32_e32 v70, 1.0, v82
	v_pk_fma_f32 v[76:77], v[20:21], v[84:85], v[76:77]
	v_rcp_f32_e32 v70, v70
	v_pk_fma_f32 v[58:59], v[24:25], v[80:81], v[76:77]
	s_nop 0
	v_mul_f32_e32 v76, 0xbfb8aa3b, v58
	v_exp_f32_e32 v76, v76
	s_nop 0
	v_add_f32_e32 v71, 1.0, v76
	v_mul_f32_e32 v76, 0xbfb8aa3b, v65
	v_exp_f32_e32 v77, v76
	v_mul_f32_e32 v76, 0xbfb8aa3b, v59
	v_exp_f32_e32 v82, v76
	v_rcp_f32_e32 v76, v71
	v_add_f32_e32 v71, 1.0, v77
	v_rcp_f32_e32 v71, v71
	v_add_f32_e32 v77, 1.0, v82
	v_rcp_f32_e32 v77, v77
	v_pk_mul_f32 v[64:65], v[64:65], v[70:71]
	s_nop 0
	v_pk_mul_f32 v[64:65], v[104:105], v[64:65]
	v_pk_mul_f32 v[58:59], v[58:59], v[76:77]
	v_bfe_u32 v76, v57, 16, 1
	v_pk_mul_f32 v[58:59], v[104:105], v[58:59]
	v_bfe_u32 v77, v56, 16, 1
	v_bfe_u32 v70, v59, 16, 1
	v_bfe_u32 v71, v58, 16, 1
	v_add3_u32 v58, v58, v71, s14
	v_add3_u32 v59, v59, v70, s14
	v_bfe_u32 v70, v60, 16, 1
	v_bfe_u32 v71, v61, 16, 1
	v_add3_u32 v56, v56, v77, s14
; __device__ __forceinline__ unsigned pk2(float lo, float hi) { return f2bf(lo) | (f2bf(hi) << 16); }
; __device__ __forceinline__ float bflo(unsigned w) { return __uint_as_float(w << 16); }
; __device__ __forceinline__ float bfhi(unsigned w) { return __uint_as_float(w & 0xffff0000u); }
; __device__ __forceinline__ float sigmoidf_(float x) { return frcp_(1.0f + fexp_(-x)); }
; __device__ __forceinline__ void p3_conv(const Args& a, const Frame& F) {
;     ...
;         for (int i = 0; i < 16; ++i) {
;             const unsigned wm[4] = {rw[i].x, rw[i].y, rw[i].z, rw[i].w}, wc_[4] = {rw[i + 1].x, rw[i + 1].y, rw[i + 1].z, rw[i + 1].w}, wp[4] = {rw[i + 2].x, rw[i + 2].y, rw[i + 2].z, rw[i + 2].w};
;             float o[8];
; #pragma unroll
;             for (int j = 0; j < 4; ++j) {
;                 const float a0 = bb[2 * j] + bflo(wm[j]) * w0[2 * j] + bflo(wc_[j]) * w1[2 * j] + bflo(wp[j]) * w2[2 * j];
;                 const float a1 = bb[2 * j + 1] + bfhi(wm[j]) * w0[2 * j + 1] + bfhi(wc_[j]) * w1[2 * j + 1] + bfhi(wp[j]) * w2[2 * j + 1];
;                 o[2 * j] = a0 * sigmoidf_(a0) * scl; o[2 * j + 1] = a1 * sigmoidf_(a1) * scl; }
;             u32x4 w; w.x = pk2(o[0], o[1]); w.y = pk2(o[2], o[3]); w.z = pk2(o[4], o[5]); w.w = pk2(o[6], o[7]);
;             *(u32x4*)(QKC + (size_t)(r0 + i) * 1024 + c0) = w;
	v_add3_u32 v57, v57, v76, s14
	v_bfe_u32 v76, v64, 16, 1
	v_bfe_u32 v77, v65, 16, 1
	v_add3_u32 v61, v61, v71, s14
	v_add3_u32 v60, v60, v70, s14
	v_add3_u32 v65, v65, v77, s14
	v_add3_u32 v64, v64, v76, s14
	v_lshrrev_b32_e32 v60, 16, v60
	v_lshrrev_b32_e32 v61, 16, v61
	v_lshrrev_b32_e32 v64, 16, v64
	v_lshrrev_b32_e32 v65, 16, v65
	v_and_or_b32 v57, v57, s13, v61
	v_and_or_b32 v56, v56, s13, v60
	v_lshlrev_b64 v[60:61], 11, v[126:127]
	v_and_or_b32 v59, v59, s13, v65
	v_and_or_b32 v58, v58, s13, v64
	v_lshl_add_u64 v[60:61], v[110:111], 0, v[60:61]
	global_store_dwordx4 v[60:61], v[56:59], off
	v_and_b32_e32 v65, 0xffff0000, v53
	v_and_b32_e32 v64, 0xffff0000, v52
	v_pk_fma_f32 v[56:57], v[10:11], v[66:67], v[6:7]
	v_lshlrev_b32_e32 v59, 16, v53
	v_pk_fma_f32 v[56:57], v[18:19], v[62:63], v[56:57]
	v_lshlrev_b32_e32 v58, 16, v52
	v_pk_fma_f32 v[56:57], v[22:23], v[58:59], v[56:57]
	v_lshlrev_b32_e32 v71, 16, v55
	v_mul_f32_e32 v60, 0xbfb8aa3b, v56
	v_exp_f32_e32 v66, v60
	v_pk_fma_f32 v[60:61], v[114:115], v[72:73], v[112:113]
	v_lshlrev_b32_e32 v70, 16, v54
	v_pk_fma_f32 v[60:61], v[4:5], v[68:69], v[60:61]
	v_and_b32_e32 v77, 0xffff0000, v55
	v_pk_fma_f32 v[52:53], v[16:17], v[64:65], v[60:61]
	v_and_b32_e32 v76, 0xffff0000, v54
	v_mul_f32_e32 v60, 0xbfb8aa3b, v52
	v_exp_f32_e32 v61, v60
	v_mul_f32_e32 v60, 0xbfb8aa3b, v57
	v_exp_f32_e32 v67, v60
	v_add_f32_e32 v60, 1.0, v66
	v_add_f32_e32 v66, 1.0, v61
	v_rcp_f32_e32 v60, v60
	v_add_f32_e32 v61, 1.0, v67
	v_mul_f32_e32 v67, 0xbfb8aa3b, v53
	v_rcp_f32_e32 v61, v61
	v_exp_f32_e32 v67, v67
	v_rcp_f32_e32 v66, v66
	v_pk_mul_f32 v[56:57], v[56:57], v[60:61]
	v_add_f32_e32 v60, 1.0, v67
	v_rcp_f32_e32 v67, v60
	v_pk_fma_f32 v[60:61], v[14:15], v[78:79], v[2:3]
	v_pk_mul_f32 v[56:57], v[104:105], v[56:57]
	v_pk_fma_f32 v[60:61], v[26:27], v[74:75], v[60:61]
	v_pk_mul_f32 v[52:53], v[52:53], v[66:67]
	v_pk_fma_f32 v[60:61], v[30:31], v[70:71], v[60:61]
	v_pk_mul_f32 v[52:53], v[104:105], v[52:53]
	v_mul_f32_e32 v72, 0xbfb8aa3b, v60
	v_exp_f32_e32 v78, v72
	v_pk_fma_f32 v[72:73], v[12:13], v[84:85], v[8:9]
	v_add_f32_e32 v66, 1.0, v78
	v_pk_fma_f32 v[72:73], v[20:21], v[80:81], v[72:73]
	v_rcp_f32_e32 v66, v66
	v_pk_fma_f32 v[54:55], v[24:25], v[76:77], v[72:73]
	s_nop 0
	v_mul_f32_e32 v72, 0xbfb8aa3b, v54
	v_exp_f32_e32 v72, v72
	s_nop 0
	v_add_f32_e32 v67, 1.0, v72
	v_mul_f32_e32 v72, 0xbfb8aa3b, v61
	v_exp_f32_e32 v73, v72
	v_mul_f32_e32 v72, 0xbfb8aa3b, v55
	v_exp_f32_e32 v78, v72
	v_rcp_f32_e32 v72, v67
	v_add_f32_e32 v67, 1.0, v73
	v_rcp_f32_e32 v67, v67
	v_add_f32_e32 v73, 1.0, v78
	v_rcp_f32_e32 v73, v73
	v_pk_mul_f32 v[60:61], v[60:61], v[66:67]
	s_nop 0
	v_pk_mul_f32 v[60:61], v[104:105], v[60:61]
	v_pk_mul_f32 v[54:55], v[54:55], v[72:73]
	v_bfe_u32 v72, v53, 16, 1
	v_pk_mul_f32 v[54:55], v[104:105], v[54:55]
	v_bfe_u32 v73, v52, 16, 1
	v_bfe_u32 v66, v55, 16, 1
	v_bfe_u32 v67, v54, 16, 1
	v_add3_u32 v54, v54, v67, s14
	v_add3_u32 v55, v55, v66, s14
	v_bfe_u32 v66, v56, 16, 1
	v_bfe_u32 v67, v57, 16, 1
	v_add3_u32 v52, v52, v73, s14
	v_add3_u32 v53, v53, v72, s14
	v_bfe_u32 v72, v60, 16, 1
	v_bfe_u32 v73, v61, 16, 1
	v_add3_u32 v57, v57, v67, s14
	v_add3_u32 v56, v56, v66, s14
	v_add3_u32 v61, v61, v73, s14
	v_add3_u32 v60, v60, v72, s14
	v_lshrrev_b32_e32 v56, 16, v56
	v_lshrrev_b32_e32 v57, 16, v57
	v_lshrrev_b32_e32 v60, 16, v60
	v_lshrrev_b32_e32 v61, 16, v61
	v_and_or_b32 v53, v53, s13, v57
	v_and_or_b32 v52, v52, s13, v56
	v_lshlrev_b64 v[56:57], 11, v[124:125]
	v_and_or_b32 v55, v55, s13, v61
	v_and_or_b32 v54, v54, s13, v60
	v_lshl_add_u64 v[56:57], v[110:111], 0, v[56:57]
	global_store_dwordx4 v[56:57], v[52:55], off
	v_and_b32_e32 v61, 0xffff0000, v49
	v_and_b32_e32 v60, 0xffff0000, v48
	v_pk_fma_f32 v[52:53], v[10:11], v[62:63], v[6:7]
	v_lshlrev_b32_e32 v55, 16, v49
	v_pk_fma_f32 v[52:53], v[18:19], v[58:59], v[52:53]
	v_lshlrev_b32_e32 v54, 16, v48
	v_pk_fma_f32 v[52:53], v[22:23], v[54:55], v[52:53]
	v_lshlrev_b32_e32 v67, 16, v51
	v_mul_f32_e32 v56, 0xbfb8aa3b, v52
	v_exp_f32_e32 v62, v56
	v_pk_fma_f32 v[56:57], v[114:115], v[68:69], v[112:113]
	v_lshlrev_b32_e32 v66, 16, v50
	v_pk_fma_f32 v[56:57], v[4:5], v[64:65], v[56:57]
	v_and_b32_e32 v73, 0xffff0000, v51
	v_pk_fma_f32 v[48:49], v[16:17], v[60:61], v[56:57]
	v_and_b32_e32 v72, 0xffff0000, v50
	v_mul_f32_e32 v56, 0xbfb8aa3b, v48
	v_exp_f32_e32 v57, v56
	v_mul_f32_e32 v56, 0xbfb8aa3b, v53
	v_exp_f32_e32 v63, v56
	v_add_f32_e32 v56, 1.0, v62
	v_add_f32_e32 v62, 1.0, v57
	v_rcp_f32_e32 v56, v56
	v_add_f32_e32 v57, 1.0, v63
	v_mul_f32_e32 v63, 0xbfb8aa3b, v49
	v_rcp_f32_e32 v57, v57
	v_exp_f32_e32 v63, v63
	v_rcp_f32_e32 v62, v62
	v_pk_mul_f32 v[52:53], v[52:53], v[56:57]
	v_add_f32_e32 v56, 1.0, v63
	v_rcp_f32_e32 v63, v56
	v_pk_fma_f32 v[56:57], v[14:15], v[74:75], v[2:3]
	v_pk_mul_f32 v[52:53], v[104:105], v[52:53]
	v_pk_fma_f32 v[56:57], v[26:27], v[70:71], v[56:57]
	v_pk_mul_f32 v[48:49], v[48:49], v[62:63]
	v_pk_fma_f32 v[56:57], v[30:31], v[66:67], v[56:57]
	v_pk_mul_f32 v[48:49], v[104:105], v[48:49]
	v_mul_f32_e32 v68, 0xbfb8aa3b, v56
	v_exp_f32_e32 v74, v68
	v_pk_fma_f32 v[68:69], v[12:13], v[80:81], v[8:9]
	v_add_f32_e32 v62, 1.0, v74
	v_pk_fma_f32 v[68:69], v[20:21], v[76:77], v[68:69]
	v_rcp_f32_e32 v62, v62
	v_pk_fma_f32 v[50:51], v[24:25], v[72:73], v[68:69]
	s_nop 0
	v_mul_f32_e32 v68, 0xbfb8aa3b, v50
	v_exp_f32_e32 v68, v68
	s_nop 0
	v_add_f32_e32 v63, 1.0, v68
	v_mul_f32_e32 v68, 0xbfb8aa3b, v57
	v_exp_f32_e32 v69, v68
	v_mul_f32_e32 v68, 0xbfb8aa3b, v51
	v_exp_f32_e32 v74, v68
	v_rcp_f32_e32 v68, v63
	v_add_f32_e32 v63, 1.0, v69
	v_rcp_f32_e32 v63, v63
	v_add_f32_e32 v69, 1.0, v74
; __device__ __forceinline__ unsigned pk2(float lo, float hi) { return f2bf(lo) | (f2bf(hi) << 16); }
; __device__ __forceinline__ float bflo(unsigned w) { return __uint_as_float(w << 16); }
; __device__ __forceinline__ float bfhi(unsigned w) { return __uint_as_float(w & 0xffff0000u); }
; __device__ __forceinline__ float sigmoidf_(float x) { return frcp_(1.0f + fexp_(-x)); }
; __device__ __forceinline__ void p3_conv(const Args& a, const Frame& F) {
;     ...
;         for (int i = 0; i < 16; ++i) {
;             const unsigned wm[4] = {rw[i].x, rw[i].y, rw[i].z, rw[i].w}, wc_[4] = {rw[i + 1].x, rw[i + 1].y, rw[i + 1].z, rw[i + 1].w}, wp[4] = {rw[i + 2].x, rw[i + 2].y, rw[i + 2].z, rw[i + 2].w};
;             float o[8];
; #pragma unroll
;             for (int j = 0; j < 4; ++j) {
;                 const float a0 = bb[2 * j] + bflo(wm[j]) * w0[2 * j] + bflo(wc_[j]) * w1[2 * j] + bflo(wp[j]) * w2[2 * j];
;                 const float a1 = bb[2 * j + 1] + bfhi(wm[j]) * w0[2 * j + 1] + bfhi(wc_[j]) * w1[2 * j + 1] + bfhi(wp[j]) * w2[2 * j + 1];
;                 o[2 * j] = a0 * sigmoidf_(a0) * scl; o[2 * j + 1] = a1 * sigmoidf_(a1) * scl; }
;             u32x4 w; w.x = pk2(o[0], o[1]); w.y = pk2(o[2], o[3]); w.z = pk2(o[4], o[5]); w.w = pk2(o[6], o[7]);
;             *(u32x4*)(QKC + (size_t)(r0 + i) * 1024 + c0) = w;
	v_rcp_f32_e32 v69, v69
	v_pk_mul_f32 v[56:57], v[56:57], v[62:63]
	s_nop 0
	v_pk_mul_f32 v[56:57], v[104:105], v[56:57]
	v_pk_mul_f32 v[50:51], v[50:51], v[68:69]
	v_bfe_u32 v68, v49, 16, 1
	v_pk_mul_f32 v[50:51], v[104:105], v[50:51]
	v_bfe_u32 v69, v48, 16, 1
	v_bfe_u32 v62, v51, 16, 1
	v_bfe_u32 v63, v50, 16, 1
	v_add3_u32 v50, v50, v63, s14
	v_add3_u32 v51, v51, v62, s14
	v_bfe_u32 v62, v52, 16, 1
	v_bfe_u32 v63, v53, 16, 1
	v_add3_u32 v48, v48, v69, s14
	v_add3_u32 v49, v49, v68, s14
	v_bfe_u32 v68, v56, 16, 1
	v_bfe_u32 v69, v57, 16, 1
	v_add3_u32 v53, v53, v63, s14
	v_add3_u32 v52, v52, v62, s14
	v_add3_u32 v57, v57, v69, s14
	v_add3_u32 v56, v56, v68, s14
	v_lshrrev_b32_e32 v52, 16, v52
	v_lshrrev_b32_e32 v53, 16, v53
	v_lshrrev_b32_e32 v56, 16, v56
	v_lshrrev_b32_e32 v57, 16, v57
	v_and_or_b32 v49, v49, s13, v53
	v_and_or_b32 v48, v48, s13, v52
	v_lshlrev_b64 v[52:53], 11, v[122:123]
	v_and_or_b32 v51, v51, s13, v57
	v_and_or_b32 v50, v50, s13, v56
	v_lshl_add_u64 v[52:53], v[110:111], 0, v[52:53]
	global_store_dwordx4 v[52:53], v[48:51], off
	v_and_b32_e32 v57, 0xffff0000, v45
	v_and_b32_e32 v56, 0xffff0000, v44
	v_pk_fma_f32 v[48:49], v[10:11], v[58:59], v[6:7]
	v_lshlrev_b32_e32 v51, 16, v45
	v_pk_fma_f32 v[48:49], v[18:19], v[54:55], v[48:49]
	v_lshlrev_b32_e32 v50, 16, v44
	v_pk_fma_f32 v[48:49], v[22:23], v[50:51], v[48:49]
	v_lshlrev_b32_e32 v63, 16, v47
	v_mul_f32_e32 v52, 0xbfb8aa3b, v48
	v_exp_f32_e32 v58, v52
	v_pk_fma_f32 v[52:53], v[114:115], v[64:65], v[112:113]
	v_lshlrev_b32_e32 v62, 16, v46
	v_pk_fma_f32 v[52:53], v[4:5], v[60:61], v[52:53]
	v_and_b32_e32 v69, 0xffff0000, v47
	v_pk_fma_f32 v[44:45], v[16:17], v[56:57], v[52:53]
	v_and_b32_e32 v68, 0xffff0000, v46
	v_mul_f32_e32 v52, 0xbfb8aa3b, v44
	v_exp_f32_e32 v53, v52
	v_mul_f32_e32 v52, 0xbfb8aa3b, v49
	v_exp_f32_e32 v59, v52
	v_add_f32_e32 v52, 1.0, v58
	v_add_f32_e32 v58, 1.0, v53
	v_rcp_f32_e32 v52, v52
	v_add_f32_e32 v53, 1.0, v59
	v_mul_f32_e32 v59, 0xbfb8aa3b, v45
	v_rcp_f32_e32 v53, v53
	v_exp_f32_e32 v59, v59
	v_rcp_f32_e32 v58, v58
	v_pk_mul_f32 v[48:49], v[48:49], v[52:53]
	v_add_f32_e32 v52, 1.0, v59
	v_rcp_f32_e32 v59, v52
	v_pk_fma_f32 v[52:53], v[14:15], v[70:71], v[2:3]
	v_pk_mul_f32 v[48:49], v[104:105], v[48:49]
	v_pk_fma_f32 v[52:53], v[26:27], v[66:67], v[52:53]
	v_pk_mul_f32 v[44:45], v[44:45], v[58:59]
	v_pk_fma_f32 v[52:53], v[30:31], v[62:63], v[52:53]
	v_pk_mul_f32 v[44:45], v[104:105], v[44:45]
	v_mul_f32_e32 v64, 0xbfb8aa3b, v52
	v_exp_f32_e32 v70, v64
	v_pk_fma_f32 v[64:65], v[12:13], v[76:77], v[8:9]
	v_add_f32_e32 v58, 1.0, v70
	v_pk_fma_f32 v[64:65], v[20:21], v[72:73], v[64:65]
	v_rcp_f32_e32 v58, v58
	v_pk_fma_f32 v[46:47], v[24:25], v[68:69], v[64:65]
	s_nop 0
	v_mul_f32_e32 v64, 0xbfb8aa3b, v46
	v_exp_f32_e32 v64, v64
	s_nop 0
	v_add_f32_e32 v59, 1.0, v64
	v_mul_f32_e32 v64, 0xbfb8aa3b, v53
	v_exp_f32_e32 v65, v64
	v_mul_f32_e32 v64, 0xbfb8aa3b, v47
	v_exp_f32_e32 v70, v64
	v_rcp_f32_e32 v64, v59
	v_add_f32_e32 v59, 1.0, v65
	v_rcp_f32_e32 v59, v59
	v_add_f32_e32 v65, 1.0, v70
	v_rcp_f32_e32 v65, v65
	v_pk_mul_f32 v[52:53], v[52:53], v[58:59]
	s_nop 0
	v_pk_mul_f32 v[52:53], v[104:105], v[52:53]
	v_pk_mul_f32 v[46:47], v[46:47], v[64:65]
	v_bfe_u32 v64, v45, 16, 1
	v_pk_mul_f32 v[46:47], v[104:105], v[46:47]
	v_bfe_u32 v65, v44, 16, 1
	v_bfe_u32 v58, v47, 16, 1
	v_bfe_u32 v59, v46, 16, 1
	v_add3_u32 v46, v46, v59, s14
	v_add3_u32 v47, v47, v58, s14
	v_bfe_u32 v58, v48, 16, 1
	v_bfe_u32 v59, v49, 16, 1
	v_add3_u32 v44, v44, v65, s14
	v_add3_u32 v45, v45, v64, s14
	v_bfe_u32 v64, v52, 16, 1
	v_bfe_u32 v65, v53, 16, 1
	v_add3_u32 v49, v49, v59, s14
	v_add3_u32 v48, v48, v58, s14
	v_add3_u32 v53, v53, v65, s14
	v_add3_u32 v52, v52, v64, s14
	v_lshrrev_b32_e32 v48, 16, v48
	v_lshrrev_b32_e32 v49, 16, v49
	v_lshrrev_b32_e32 v52, 16, v52
	v_lshrrev_b32_e32 v53, 16, v53
	v_and_or_b32 v45, v45, s13, v49
	v_and_or_b32 v44, v44, s13, v48
	v_lshlrev_b64 v[48:49], 11, v[120:121]
	v_and_or_b32 v47, v47, s13, v53
	v_and_or_b32 v46, v46, s13, v52
	v_lshl_add_u64 v[48:49], v[110:111], 0, v[48:49]
	global_store_dwordx4 v[48:49], v[44:47], off
	v_and_b32_e32 v53, 0xffff0000, v41
	v_and_b32_e32 v52, 0xffff0000, v40
	v_pk_fma_f32 v[44:45], v[10:11], v[54:55], v[6:7]
	v_lshlrev_b32_e32 v47, 16, v41
	v_pk_fma_f32 v[44:45], v[18:19], v[50:51], v[44:45]
	v_lshlrev_b32_e32 v46, 16, v40
	v_pk_fma_f32 v[44:45], v[22:23], v[46:47], v[44:45]
	v_lshlrev_b32_e32 v59, 16, v43
	v_mul_f32_e32 v48, 0xbfb8aa3b, v44
	v_exp_f32_e32 v54, v48
	v_pk_fma_f32 v[48:49], v[114:115], v[60:61], v[112:113]
	v_lshlrev_b32_e32 v58, 16, v42
	v_pk_fma_f32 v[48:49], v[4:5], v[56:57], v[48:49]
	v_and_b32_e32 v65, 0xffff0000, v43
	v_pk_fma_f32 v[40:41], v[16:17], v[52:53], v[48:49]
	v_and_b32_e32 v64, 0xffff0000, v42
	v_mul_f32_e32 v48, 0xbfb8aa3b, v40
	v_exp_f32_e32 v49, v48
	v_mul_f32_e32 v48, 0xbfb8aa3b, v45
	v_exp_f32_e32 v55, v48
	v_add_f32_e32 v48, 1.0, v54
	v_add_f32_e32 v54, 1.0, v49
	v_rcp_f32_e32 v48, v48
	v_add_f32_e32 v49, 1.0, v55
	v_mul_f32_e32 v55, 0xbfb8aa3b, v41
	v_rcp_f32_e32 v49, v49
	v_exp_f32_e32 v55, v55
	v_rcp_f32_e32 v54, v54
	v_pk_mul_f32 v[44:45], v[44:45], v[48:49]
	v_add_f32_e32 v48, 1.0, v55
	v_rcp_f32_e32 v55, v48
	v_pk_fma_f32 v[48:49], v[14:15], v[66:67], v[2:3]
	v_pk_mul_f32 v[44:45], v[104:105], v[44:45]
	v_pk_fma_f32 v[48:49], v[26:27], v[62:63], v[48:49]
	v_pk_mul_f32 v[40:41], v[40:41], v[54:55]
	v_pk_fma_f32 v[48:49], v[30:31], v[58:59], v[48:49]
	v_pk_mul_f32 v[40:41], v[104:105], v[40:41]
	v_mul_f32_e32 v60, 0xbfb8aa3b, v48
	v_exp_f32_e32 v66, v60
	v_pk_fma_f32 v[60:61], v[12:13], v[72:73], v[8:9]
	v_add_f32_e32 v54, 1.0, v66
; __device__ __forceinline__ unsigned pk2(float lo, float hi) { return f2bf(lo) | (f2bf(hi) << 16); }
; __device__ __forceinline__ float bflo(unsigned w) { return __uint_as_float(w << 16); }
; __device__ __forceinline__ float bfhi(unsigned w) { return __uint_as_float(w & 0xffff0000u); }
; __device__ __forceinline__ float sigmoidf_(float x) { return frcp_(1.0f + fexp_(-x)); }
; __device__ __forceinline__ void p3_conv(const Args& a, const Frame& F) {
;     ...
;         for (int i = 0; i < 16; ++i) {
;             const unsigned wm[4] = {rw[i].x, rw[i].y, rw[i].z, rw[i].w}, wc_[4] = {rw[i + 1].x, rw[i + 1].y, rw[i + 1].z, rw[i + 1].w}, wp[4] = {rw[i + 2].x, rw[i + 2].y, rw[i + 2].z, rw[i + 2].w};
;             float o[8];
; #pragma unroll
;             for (int j = 0; j < 4; ++j) {
;                 const float a0 = bb[2 * j] + bflo(wm[j]) * w0[2 * j] + bflo(wc_[j]) * w1[2 * j] + bflo(wp[j]) * w2[2 * j];
;                 const float a1 = bb[2 * j + 1] + bfhi(wm[j]) * w0[2 * j + 1] + bfhi(wc_[j]) * w1[2 * j + 1] + bfhi(wp[j]) * w2[2 * j + 1];
;                 o[2 * j] = a0 * sigmoidf_(a0) * scl; o[2 * j + 1] = a1 * sigmoidf_(a1) * scl; }
;             u32x4 w; w.x = pk2(o[0], o[1]); w.y = pk2(o[2], o[3]); w.z = pk2(o[4], o[5]); w.w = pk2(o[6], o[7]);
;             *(u32x4*)(QKC + (size_t)(r0 + i) * 1024 + c0) = w;
	v_pk_fma_f32 v[60:61], v[20:21], v[68:69], v[60:61]
	v_rcp_f32_e32 v54, v54
	v_pk_fma_f32 v[42:43], v[24:25], v[64:65], v[60:61]
	s_nop 0
	v_mul_f32_e32 v60, 0xbfb8aa3b, v42
	v_exp_f32_e32 v60, v60
	s_nop 0
	v_add_f32_e32 v55, 1.0, v60
	v_mul_f32_e32 v60, 0xbfb8aa3b, v49
	v_exp_f32_e32 v61, v60
	v_mul_f32_e32 v60, 0xbfb8aa3b, v43
	v_exp_f32_e32 v66, v60
	v_rcp_f32_e32 v60, v55
	v_add_f32_e32 v55, 1.0, v61
	v_rcp_f32_e32 v55, v55
	v_add_f32_e32 v61, 1.0, v66
	v_rcp_f32_e32 v61, v61
	v_pk_mul_f32 v[48:49], v[48:49], v[54:55]
	s_nop 0
	v_pk_mul_f32 v[48:49], v[104:105], v[48:49]
	v_pk_mul_f32 v[42:43], v[42:43], v[60:61]
	v_bfe_u32 v60, v41, 16, 1
	v_pk_mul_f32 v[42:43], v[104:105], v[42:43]
	v_bfe_u32 v61, v40, 16, 1
	v_bfe_u32 v54, v43, 16, 1
	v_bfe_u32 v55, v42, 16, 1
	v_add3_u32 v42, v42, v55, s14
	v_add3_u32 v43, v43, v54, s14
	v_bfe_u32 v54, v44, 16, 1
	v_bfe_u32 v55, v45, 16, 1
	v_add3_u32 v40, v40, v61, s14
	v_add3_u32 v41, v41, v60, s14
	v_bfe_u32 v60, v48, 16, 1
	v_bfe_u32 v61, v49, 16, 1
	v_add3_u32 v45, v45, v55, s14
	v_add3_u32 v44, v44, v54, s14
	v_add3_u32 v49, v49, v61, s14
	v_add3_u32 v48, v48, v60, s14
	v_lshrrev_b32_e32 v44, 16, v44
	v_lshrrev_b32_e32 v45, 16, v45
	v_lshrrev_b32_e32 v48, 16, v48
	v_lshrrev_b32_e32 v49, 16, v49
	v_and_or_b32 v41, v41, s13, v45
	v_and_or_b32 v40, v40, s13, v44
	v_lshlrev_b64 v[44:45], 11, v[118:119]
	v_and_or_b32 v43, v43, s13, v49
	v_and_or_b32 v42, v42, s13, v48
	v_lshl_add_u64 v[44:45], v[110:111], 0, v[44:45]
	global_store_dwordx4 v[44:45], v[40:43], off
	v_and_b32_e32 v49, 0xffff0000, v37
	v_and_b32_e32 v48, 0xffff0000, v36
	v_pk_fma_f32 v[40:41], v[10:11], v[50:51], v[6:7]
	v_lshlrev_b32_e32 v43, 16, v37
	v_pk_fma_f32 v[40:41], v[18:19], v[46:47], v[40:41]
	v_lshlrev_b32_e32 v42, 16, v36
	v_pk_fma_f32 v[40:41], v[22:23], v[42:43], v[40:41]
	v_lshlrev_b32_e32 v55, 16, v39
	v_mul_f32_e32 v44, 0xbfb8aa3b, v40
	v_exp_f32_e32 v50, v44
	v_pk_fma_f32 v[44:45], v[114:115], v[56:57], v[112:113]
	v_lshlrev_b32_e32 v54, 16, v38
	v_pk_fma_f32 v[44:45], v[4:5], v[52:53], v[44:45]
	v_and_b32_e32 v61, 0xffff0000, v39
	v_pk_fma_f32 v[36:37], v[16:17], v[48:49], v[44:45]
	v_and_b32_e32 v60, 0xffff0000, v38
	v_mul_f32_e32 v44, 0xbfb8aa3b, v36
	v_exp_f32_e32 v45, v44
	v_mul_f32_e32 v44, 0xbfb8aa3b, v41
	v_exp_f32_e32 v51, v44
	v_add_f32_e32 v44, 1.0, v50
	v_add_f32_e32 v50, 1.0, v45
	v_rcp_f32_e32 v44, v44
	v_add_f32_e32 v45, 1.0, v51
	v_mul_f32_e32 v51, 0xbfb8aa3b, v37
	v_rcp_f32_e32 v45, v45
	v_exp_f32_e32 v51, v51
	v_rcp_f32_e32 v50, v50
	v_pk_mul_f32 v[40:41], v[40:41], v[44:45]
	v_add_f32_e32 v44, 1.0, v51
	v_rcp_f32_e32 v51, v44
	v_pk_fma_f32 v[44:45], v[14:15], v[62:63], v[2:3]
	v_pk_mul_f32 v[40:41], v[104:105], v[40:41]
	v_pk_fma_f32 v[44:45], v[26:27], v[58:59], v[44:45]
	v_pk_mul_f32 v[36:37], v[36:37], v[50:51]
	v_pk_fma_f32 v[44:45], v[30:31], v[54:55], v[44:45]
	v_pk_mul_f32 v[36:37], v[104:105], v[36:37]
	v_mul_f32_e32 v56, 0xbfb8aa3b, v44
	v_exp_f32_e32 v62, v56
	v_pk_fma_f32 v[56:57], v[12:13], v[68:69], v[8:9]
	v_add_f32_e32 v50, 1.0, v62
	v_pk_fma_f32 v[56:57], v[20:21], v[64:65], v[56:57]
	v_rcp_f32_e32 v50, v50
	v_pk_fma_f32 v[38:39], v[24:25], v[60:61], v[56:57]
	s_nop 0
	v_mul_f32_e32 v56, 0xbfb8aa3b, v38
	v_exp_f32_e32 v56, v56
	s_nop 0
	v_add_f32_e32 v51, 1.0, v56
	v_mul_f32_e32 v56, 0xbfb8aa3b, v45
	v_exp_f32_e32 v57, v56
	v_mul_f32_e32 v56, 0xbfb8aa3b, v39
	v_exp_f32_e32 v62, v56
	v_rcp_f32_e32 v56, v51
	v_add_f32_e32 v51, 1.0, v57
	v_rcp_f32_e32 v51, v51
	v_add_f32_e32 v57, 1.0, v62
	v_rcp_f32_e32 v57, v57
	v_pk_mul_f32 v[44:45], v[44:45], v[50:51]
	s_nop 0
	v_pk_mul_f32 v[44:45], v[104:105], v[44:45]
	v_pk_mul_f32 v[38:39], v[38:39], v[56:57]
	v_bfe_u32 v56, v37, 16, 1
	v_pk_mul_f32 v[38:39], v[104:105], v[38:39]
	v_bfe_u32 v57, v36, 16, 1
	v_bfe_u32 v50, v39, 16, 1
; __device__ __forceinline__ unsigned pk2(float lo, float hi) { return f2bf(lo) | (f2bf(hi) << 16); }
; __device__ __forceinline__ float bflo(unsigned w) { return __uint_as_float(w << 16); }
; __device__ __forceinline__ float bfhi(unsigned w) { return __uint_as_float(w & 0xffff0000u); }
; __device__ __forceinline__ float sigmoidf_(float x) { return frcp_(1.0f + fexp_(-x)); }
; __device__ __forceinline__ void p3_conv(const Args& a, const Frame& F) {
;     ...
;         for (int i = 0; i < 16; ++i) {
;             const unsigned wm[4] = {rw[i].x, rw[i].y, rw[i].z, rw[i].w}, wc_[4] = {rw[i + 1].x, rw[i + 1].y, rw[i + 1].z, rw[i + 1].w}, wp[4] = {rw[i + 2].x, rw[i + 2].y, rw[i + 2].z, rw[i + 2].w};
;             float o[8];
; #pragma unroll
;             for (int j = 0; j < 4; ++j) {
;                 const float a0 = bb[2 * j] + bflo(wm[j]) * w0[2 * j] + bflo(wc_[j]) * w1[2 * j] + bflo(wp[j]) * w2[2 * j];
;                 const float a1 = bb[2 * j + 1] + bfhi(wm[j]) * w0[2 * j + 1] + bfhi(wc_[j]) * w1[2 * j + 1] + bfhi(wp[j]) * w2[2 * j + 1];
;                 o[2 * j] = a0 * sigmoidf_(a0) * scl; o[2 * j + 1] = a1 * sigmoidf_(a1) * scl; }
;             u32x4 w; w.x = pk2(o[0], o[1]); w.y = pk2(o[2], o[3]); w.z = pk2(o[4], o[5]); w.w = pk2(o[6], o[7]);
;             *(u32x4*)(QKC + (size_t)(r0 + i) * 1024 + c0) = w;
	v_bfe_u32 v51, v38, 16, 1
	v_add3_u32 v38, v38, v51, s14
	v_add3_u32 v39, v39, v50, s14
	v_bfe_u32 v50, v40, 16, 1
	v_bfe_u32 v51, v41, 16, 1
	v_add3_u32 v36, v36, v57, s14
	v_add3_u32 v37, v37, v56, s14
	v_bfe_u32 v56, v44, 16, 1
	v_bfe_u32 v57, v45, 16, 1
	v_add3_u32 v41, v41, v51, s14
	v_add3_u32 v40, v40, v50, s14
	v_add3_u32 v45, v45, v57, s14
	v_add3_u32 v44, v44, v56, s14
	v_lshrrev_b32_e32 v40, 16, v40
	v_lshrrev_b32_e32 v41, 16, v41
	v_lshrrev_b32_e32 v44, 16, v44
	v_lshrrev_b32_e32 v45, 16, v45
	v_and_or_b32 v37, v37, s13, v41
	v_and_or_b32 v36, v36, s13, v40
	v_lshlrev_b64 v[40:41], 11, v[116:117]
	v_and_or_b32 v39, v39, s13, v45
	v_and_or_b32 v38, v38, s13, v44
	v_lshl_add_u64 v[40:41], v[110:111], 0, v[40:41]
	global_store_dwordx4 v[40:41], v[36:39], off
	s_nop 1
	v_pk_fma_f32 v[36:37], v[10:11], v[46:47], v[6:7]
	v_lshlrev_b32_e32 v39, 16, v33
	v_pk_fma_f32 v[36:37], v[18:19], v[42:43], v[36:37]
	v_lshlrev_b32_e32 v38, 16, v32
	v_pk_fma_f32 v[36:37], v[22:23], v[38:39], v[36:37]
	v_and_b32_e32 v33, 0xffff0000, v33
	v_mul_f32_e32 v38, 0xbfb8aa3b, v36
	v_exp_f32_e32 v40, v38
	v_pk_fma_f32 v[38:39], v[114:115], v[52:53], v[112:113]
	v_and_b32_e32 v32, 0xffff0000, v32
	v_pk_fma_f32 v[38:39], v[4:5], v[48:49], v[38:39]
	v_lshlrev_b32_e32 v43, 16, v35
	v_pk_fma_f32 v[32:33], v[16:17], v[32:33], v[38:39]
	v_lshlrev_b32_e32 v42, 16, v34
	v_mul_f32_e32 v38, 0xbfb8aa3b, v32
	v_exp_f32_e32 v39, v38
	v_mul_f32_e32 v38, 0xbfb8aa3b, v37
	v_exp_f32_e32 v41, v38
	v_add_f32_e32 v38, 1.0, v40
	v_add_f32_e32 v40, 1.0, v39
	v_rcp_f32_e32 v38, v38
	v_add_f32_e32 v39, 1.0, v41
	v_mul_f32_e32 v41, 0xbfb8aa3b, v33
	v_rcp_f32_e32 v39, v39
	v_exp_f32_e32 v41, v41
	v_and_b32_e32 v35, 0xffff0000, v35
	v_and_b32_e32 v34, 0xffff0000, v34
	v_pk_mul_f32 v[36:37], v[36:37], v[38:39]
	v_add_f32_e32 v38, 1.0, v41
	v_rcp_f32_e32 v41, v38
	v_pk_fma_f32 v[38:39], v[14:15], v[58:59], v[2:3]
	v_rcp_f32_e32 v40, v40
	v_pk_fma_f32 v[38:39], v[26:27], v[54:55], v[38:39]
	v_pk_mul_f32 v[36:37], v[104:105], v[36:37]
	v_pk_fma_f32 v[38:39], v[30:31], v[42:43], v[38:39]
	v_pk_mul_f32 v[32:33], v[32:33], v[40:41]
	v_mul_f32_e32 v42, 0xbfb8aa3b, v38
	v_exp_f32_e32 v44, v42
	v_pk_fma_f32 v[42:43], v[12:13], v[64:65], v[8:9]
	v_pk_mul_f32 v[32:33], v[104:105], v[32:33]
	v_pk_fma_f32 v[42:43], v[20:21], v[60:61], v[42:43]
	v_add_f32_e32 v40, 1.0, v44
	v_pk_fma_f32 v[34:35], v[24:25], v[34:35], v[42:43]
	v_rcp_f32_e32 v40, v40
	v_mul_f32_e32 v42, 0xbfb8aa3b, v34
	v_exp_f32_e32 v42, v42
	s_nop 0
	v_add_f32_e32 v41, 1.0, v42
	v_mul_f32_e32 v42, 0xbfb8aa3b, v39
	v_exp_f32_e32 v43, v42
	v_mul_f32_e32 v42, 0xbfb8aa3b, v35
	v_exp_f32_e32 v44, v42
	v_rcp_f32_e32 v42, v41
	v_add_f32_e32 v41, 1.0, v43
	v_rcp_f32_e32 v41, v41
	v_add_f32_e32 v43, 1.0, v44
	v_rcp_f32_e32 v43, v43
	v_pk_mul_f32 v[38:39], v[38:39], v[40:41]
	s_nop 0
	v_pk_mul_f32 v[38:39], v[104:105], v[38:39]
	v_pk_mul_f32 v[34:35], v[34:35], v[42:43]
	v_bfe_u32 v42, v33, 16, 1
	v_pk_mul_f32 v[34:35], v[104:105], v[34:35]
	v_bfe_u32 v43, v32, 16, 1
	v_bfe_u32 v40, v35, 16, 1
	v_bfe_u32 v41, v34, 16, 1
	v_add3_u32 v32, v32, v43, s14
	v_add3_u32 v33, v33, v42, s14
	v_add3_u32 v34, v34, v41, s14
	v_add3_u32 v35, v35, v40, s14
	v_bfe_u32 v40, v36, 16, 1
	v_bfe_u32 v41, v37, 16, 1
	v_bfe_u32 v42, v38, 16, 1
	v_bfe_u32 v43, v39, 16, 1
	v_add3_u32 v39, v39, v43, s14
	v_add3_u32 v38, v38, v42, s14
	v_add3_u32 v37, v37, v41, s14
	v_add3_u32 v36, v36, v40, s14
	v_lshrrev_b32_e32 v36, 16, v36
	v_lshrrev_b32_e32 v37, 16, v37
	v_lshrrev_b32_e32 v38, 16, v38
	v_lshrrev_b32_e32 v39, 16, v39
	v_and_or_b32 v35, v35, s13, v39
	v_and_or_b32 v34, v34, s13, v38
	v_and_or_b32 v33, v33, s13, v37
	v_and_or_b32 v32, v32, s13, v36
	global_store_dwordx4 v[28:29], v[32:35], off
	s_andn2_b64 exec, exec, s[6:7]
	s_cbranch_execz .LBB0_380
